# gather: each wave raises its priority (s_setprio 2) for the serial butterfly+gelu chain of a group step and drops to 0 for the bulk 4-bit decode/FMA part
# speedup vs baseline: 1.0049x; 1.0049x over previous
.LBB0_763:
	s_cmpk_eq_i32 s58, 0x80
	s_cselect_b64 s[12:13], -1, 0
	ds_bpermute_b32 v84, v93, v92
	s_and_b64 vcc, s[12:13], s[48:49]
	v_cndmask_b32_e32 v104, v0, v94, vcc
	v_ashrrev_i32_e32 v105, 31, v104
	s_and_b32 s12, s58, 0x70
	v_lshlrev_b64 v[104:105], 9, v[104:105]
	v_lshl_add_u64 v[104:105], s[94:95], 0, v[104:105]
	s_lshl_b32 s36, s12, 2
	s_waitcnt lgkmcnt(0)
	v_ashrrev_i32_e32 v85, 31, v84
	v_lshl_add_u64 v[104:105], v[104:105], 0, s[36:37]
	v_lshl_add_u64 v[84:85], v[84:85], 3, s[8:9]
	v_lshl_add_u64 v[104:105], v[104:105], 0, v[144:145]
	global_load_dwordx2 v[84:85], v[84:85], off
	s_nop 0
	global_load_dword v86, v[72:73], off
	global_load_dword v92, v[104:105], off
	s_waitcnt vmcnt(11)
	v_dot8_i32_i4 v87, v8, v1, 0
	v_dot8_i32_i4 v104, v8, v88, 0
	v_dot8_i32_i4 v87, v9, v89, v87
	v_dot8_i32_i4 v104, v9, v90, v104
	s_waitcnt vmcnt(10)
	v_dot8_i32_i4 v9, v10, v88, 0
	v_dot8_i32_i4 v9, v11, v90, v9
	v_lshl_add_u32 v87, v87, 4, v104
	v_dot8_i32_i4 v8, v10, v1, 0
	v_dot8_i32_i4 v8, v11, v89, v8
	s_add_i32 s58, s58, 16
	v_lshl_add_u64 v[72:73], v[72:73], 0, 64
	s_waitcnt vmcnt(2)
	v_mul_f32_e32 v85, v91, v85
	v_lshl_add_u32 v104, v8, 4, v9
	v_dot8_i32_i4 v8, v12, v1, 0
	v_dot8_i32_i4 v9, v12, v88, 0
	v_dot8_i32_i4 v8, v13, v89, v8
	v_dot8_i32_i4 v9, v13, v90, v9
	s_waitcnt vmcnt(0)
	v_readlane_b32 s12, v92, 0
	v_readlane_b32 s28, v92, 8
	v_readlane_b32 s30, v92, 9
	v_lshl_add_u32 v105, v8, 4, v9
	v_dot8_i32_i4 v8, v14, v1, 0
	v_dot8_i32_i4 v9, v14, v88, 0
	v_dot8_i32_i4 v8, v15, v89, v8
	v_dot8_i32_i4 v9, v15, v90, v9
	s_ashr_i32 s13, s12, 31
	v_readlane_b32 s14, v92, 1
	s_ashr_i32 s29, s28, 31
	v_lshl_add_u32 v106, v8, 4, v9
	v_dot8_i32_i4 v8, v16, v1, 0
	v_dot8_i32_i4 v9, v16, v88, 0
	v_dot8_i32_i4 v8, v17, v89, v8
	v_dot8_i32_i4 v9, v17, v90, v9
	s_ashr_i32 s31, s30, 31
	v_readlane_b32 s34, v92, 10
	s_lshl_b64 s[12:13], s[12:13], 9
	v_lshl_add_u32 v107, v8, 4, v9
	v_dot8_i32_i4 v8, v18, v1, 0
	v_dot8_i32_i4 v9, v18, v88, 0
	v_dot8_i32_i4 v8, v19, v89, v8
	v_dot8_i32_i4 v9, v19, v90, v9
	s_ashr_i32 s15, s14, 31
	v_readlane_b32 s16, v92, 2
	s_lshl_b64 s[28:29], s[28:29], 9
	v_lshl_add_u32 v108, v8, 4, v9
	v_dot8_i32_i4 v8, v20, v1, 0
	v_dot8_i32_i4 v9, v20, v88, 0
	v_dot8_i32_i4 v8, v21, v89, v8
	v_dot8_i32_i4 v9, v21, v90, v9
	s_lshl_b64 s[30:31], s[30:31], 9
	s_ashr_i32 s35, s34, 31
	v_readlane_b32 s38, v92, 11
	v_lshl_add_u32 v109, v8, 4, v9
	v_dot8_i32_i4 v8, v22, v1, 0
	v_dot8_i32_i4 v9, v22, v88, 0
	v_dot8_i32_i4 v8, v23, v89, v8
	v_dot8_i32_i4 v9, v23, v90, v9
	s_lshl_b64 s[14:15], s[14:15], 9
	s_ashr_i32 s17, s16, 31
	v_readlane_b32 s18, v92, 3
	v_lshl_add_u32 v110, v8, 4, v9
	v_dot8_i32_i4 v8, v24, v1, 0
	v_dot8_i32_i4 v9, v24, v88, 0
	v_dot8_i32_i4 v8, v25, v89, v8
	v_dot8_i32_i4 v9, v25, v90, v9
	s_lshl_b64 s[34:35], s[34:35], 9
	s_ashr_i32 s39, s38, 31
	s_nop 0
	v_lshl_add_u32 v111, v8, 4, v9
	v_dot8_i32_i4 v8, v38, v1, 0
	v_dot8_i32_i4 v9, v38, v88, 0
	v_dot8_i32_i4 v8, v39, v89, v8
	v_dot8_i32_i4 v9, v39, v90, v9
	s_setprio 2
	v_permlane32_swap_b32 v87, v111
	s_nop 1
	v_lshl_add_u32 v112, v8, 4, v9
	v_dot8_i32_i4 v8, v50, v1, 0
	v_dot8_i32_i4 v9, v50, v88, 0
	v_dot8_i32_i4 v8, v51, v89, v8
	v_dot8_i32_i4 v9, v51, v90, v9
	s_waitcnt lgkmcnt(0)
	v_add_u32_e32 v87, v87, v111
	v_permlane32_swap_b32 v104, v112
	v_lshl_add_u32 v113, v8, 4, v9
	v_dot8_i32_i4 v8, v48, v1, 0
	v_dot8_i32_i4 v9, v48, v88, 0
	v_dot8_i32_i4 v8, v49, v89, v8
	v_dot8_i32_i4 v9, v49, v90, v9
	s_waitcnt lgkmcnt(0)
	v_add_u32_e32 v104, v104, v112
	v_permlane32_swap_b32 v105, v113
	v_lshl_add_u32 v114, v8, 4, v9
	v_dot8_i32_i4 v8, v46, v1, 0
	v_dot8_i32_i4 v9, v46, v88, 0
	v_dot8_i32_i4 v8, v47, v89, v8
	v_dot8_i32_i4 v9, v47, v90, v9
	s_waitcnt lgkmcnt(0)
	v_add_u32_e32 v105, v105, v113
	v_permlane32_swap_b32 v106, v114
	v_lshl_add_u32 v115, v8, 4, v9
	v_dot8_i32_i4 v8, v44, v1, 0
	v_dot8_i32_i4 v9, v44, v88, 0
	v_dot8_i32_i4 v8, v45, v89, v8
	v_dot8_i32_i4 v9, v45, v90, v9
	s_waitcnt lgkmcnt(0)
	v_add_u32_e32 v106, v106, v114
	v_permlane32_swap_b32 v107, v115
	v_lshl_add_u32 v116, v8, 4, v9
	v_dot8_i32_i4 v8, v42, v1, 0
	v_dot8_i32_i4 v9, v42, v88, 0
	v_dot8_i32_i4 v8, v43, v89, v8
	v_dot8_i32_i4 v9, v43, v90, v9
	s_waitcnt lgkmcnt(0)
	v_add_u32_e32 v107, v107, v115
	v_permlane32_swap_b32 v108, v116
	v_lshl_add_u32 v117, v8, 4, v9
	v_dot8_i32_i4 v8, v40, v1, 0
	v_dot8_i32_i4 v9, v40, v88, 0
	v_dot8_i32_i4 v8, v41, v89, v8
	v_dot8_i32_i4 v9, v41, v90, v9
	s_waitcnt lgkmcnt(0)
	v_add_u32_e32 v108, v108, v116
	v_permlane32_swap_b32 v109, v117
	v_lshl_add_u32 v118, v8, 4, v9
	s_waitcnt lgkmcnt(0)
	v_add_u32_e32 v109, v109, v117
	v_permlane32_swap_b32 v110, v118
	v_readlane_b32 s50, v92, 12
	s_lshl_b64 s[16:17], s[16:17], 9
	s_ashr_i32 s19, s18, 31
	s_waitcnt lgkmcnt(0)
	v_add_u32_e32 v110, v110, v118
	v_permlane16_swap_b32 v87, v107
	v_readlane_b32 s20, v92, 4
	s_add_u32 s66, s28, s62
	s_addc_u32 s67, s29, s63
	global_load_dwordx2 v[24:25], v121, s[66:67]
	s_add_u32 s66, s30, s62
	s_addc_u32 s67, s31, s63
	global_load_dwordx2 v[38:39], v121, s[66:67]
	s_waitcnt lgkmcnt(0)
	v_add_u32_e32 v87, v87, v107
	v_permlane16_swap_b32 v104, v108
	s_lshl_b64 s[38:39], s[38:39], 9
	s_ashr_i32 s51, s50, 31
	v_readlane_b32 s52, v92, 13
	s_waitcnt lgkmcnt(0)
	v_add_u32_e32 v104, v104, v108
	v_permlane16_swap_b32 v105, v109
	s_lshl_b64 s[18:19], s[18:19], 9
	s_ashr_i32 s21, s20, 31
	v_readlane_b32 s22, v92, 5
	s_waitcnt lgkmcnt(0)
	v_add_u32_e32 v105, v105, v109
	v_permlane16_swap_b32 v106, v110
	s_add_u32 s66, s34, s62
	s_addc_u32 s67, s35, s63
	global_load_dwordx2 v[50:51], v121, s[66:67]
	s_lshl_b64 s[50:51], s[50:51], 9
	s_ashr_i32 s53, s52, 31
	s_waitcnt lgkmcnt(0)
	v_add_u32_e32 v106, v106, v110
	v_cndmask_b32_e64 v107, v87, v105, s[44:45]
	v_cndmask_b32_e64 v87, v105, v87, s[44:45]
	s_nop 0
	v_readlane_b32 s54, v92, 14
	s_lshl_b64 s[20:21], s[20:21], 9
	s_ashr_i32 s23, s22, 31
	v_readlane_b32 s24, v92, 6
	s_waitcnt lgkmcnt(0)
	v_add_u32_dpp v87, v107, v87 row_ror:8 row_mask:0xf bank_mask:0xf
	v_cndmask_b32_e64 v105, v104, v106, s[44:45]
	s_nop 1
	v_cndmask_b32_e64 v104, v106, v104, s[44:45]
	s_lshl_b64 s[52:53], s[52:53], 9
	s_ashr_i32 s55, s54, 31
	v_readlane_b32 s56, v92, 15
	s_waitcnt lgkmcnt(0)
	v_add_u32_dpp v104, v105, v104 row_ror:8 row_mask:0xf bank_mask:0xf
	v_cndmask_b32_e64 v105, v87, v104, s[46:47]
	v_cndmask_b32_e64 v87, v104, v87, s[46:47]
	s_nop 0
	v_mov_b32_dpp v104, v105 row_half_mirror row_mask:0xf bank_mask:0xf
	s_nop 1
	s_lshl_b64 s[22:23], s[22:23], 9
	s_ashr_i32 s25, s24, 31
	v_readlane_b32 s26, v92, 7
	s_lshl_b64 s[54:55], s[54:55], 9
	s_waitcnt lgkmcnt(0)
	v_add_u32_dpp v87, v104, v87 quad_perm:[3,2,1,0] row_mask:0xf bank_mask:0xf
	s_nop 1
	s_ashr_i32 s57, s56, 31
	s_lshl_b64 s[24:25], s[24:25], 9
	s_ashr_i32 s27, s26, 31
	s_lshl_b64 s[56:57], s[56:57], 9
	s_waitcnt lgkmcnt(0)
	v_add_u32_dpp v87, v87, v87 quad_perm:[2,3,0,1] row_mask:0xf bank_mask:0xf
	s_nop 1
	s_lshl_b64 s[26:27], s[26:27], 9
	s_waitcnt lgkmcnt(0)
	v_add_u32_dpp v87, v87, v87 quad_perm:[1,0,3,2] row_mask:0xf bank_mask:0xf
	v_cvt_f32_i32_e32 v87, v87
	v_add_f32_e32 v87, v95, v87
	v_mul_f32_e32 v85, v85, v87
	v_mul_f32_e32 v87, 0x3d372713, v85
	v_mul_f32_e32 v87, v85, v87
	v_fma_f32 v87, v85, v87, v85
	v_mul_f32_e32 v87, 0x3fcc422a, v87
	v_mul_f32_e32 v87, 0xbfb8aa3b, v87
	v_exp_f32_e32 v87, v87
	s_nop 0
	v_add_f32_e32 v87, 1.0, v87
	v_rcp_f32_e32 v87, v87
	s_nop 0
	v_pk_mul_f32 v[84:85], v[84:85], v[86:87]
	v_alignbit_b32 v224, v82, v82, 4
	v_pk_mul_f32 v[84:85], v[84:85], v[84:85] op_sel:[0,1] op_sel_hi:[1,0]
	v_cvt_f16_f32_e32 v120, v84
	s_setprio 0
	v_and_b32_e32 v86, 0x7070707, v82
	v_readlane_b32 s36, v120, 0
	v_and_b32_e32 v87, 0x7070707, v224
	v_perm_b32 v86, s2, v205, v86
	v_perm_b32 v87, s2, v205, v87
	v_and_or_b32 v86, v82, s4, v86
	v_and_or_b32 v82, v224, s4, v87
	v_perm_b32 v87, v82, v86, s5
	v_perm_b32 v104, v82, v86, s33
	v_perm_b32 v105, v82, v86, s0
	v_perm_b32 v82, v82, v86, s1
	v_pk_fma_f16 v86, v87, s36, v103 op_sel_hi:[1,0,1]
	v_pk_fma_f16 v87, v104, s36, v102 op_sel_hi:[1,0,1]
	v_alignbit_b32 v225, v83, v83, 4
	v_pk_fma_f16 v82, v82, s36, v100 op_sel_hi:[1,0,1]
	v_and_b32_e32 v100, 0x7070707, v83
	v_and_b32_e32 v102, 0x7070707, v225
	v_perm_b32 v100, s2, v205, v100
	v_perm_b32 v102, s2, v205, v102
	v_and_or_b32 v100, v83, s4, v100
	v_and_or_b32 v83, v225, s4, v102
	v_perm_b32 v102, v83, v100, s5
	v_perm_b32 v103, v83, v100, s33
	v_perm_b32 v104, v83, v100, s0
	v_perm_b32 v83, v83, v100, s1
	v_readlane_b32 s59, v120, 4
	v_alignbit_b32 v224, v80, v80, 4
	v_pk_fma_f16 v101, v105, s36, v101 op_sel_hi:[1,0,1]
	v_pk_fma_f16 v99, v102, s36, v99 op_sel_hi:[1,0,1]
	v_pk_fma_f16 v98, v103, s36, v98 op_sel_hi:[1,0,1]
	v_pk_fma_f16 v97, v104, s36, v97 op_sel_hi:[1,0,1]
	v_pk_fma_f16 v83, v83, s36, v96 op_sel_hi:[1,0,1]
	v_and_b32_e32 v96, 0x7070707, v80
	v_and_b32_e32 v100, 0x7070707, v224
	v_perm_b32 v96, s2, v205, v96
	v_perm_b32 v100, s2, v205, v100
	v_and_or_b32 v96, v80, s4, v96
	v_and_or_b32 v80, v224, s4, v100
	v_perm_b32 v100, v80, v96, s5
	v_perm_b32 v102, v80, v96, s33
	v_perm_b32 v103, v80, v96, s0
	v_perm_b32 v80, v80, v96, s1
	v_pk_fma_f16 v86, v100, s59, v86 op_sel_hi:[1,0,1]
	v_alignbit_b32 v225, v81, v81, 4
	v_pk_fma_f16 v80, v80, s59, v82 op_sel_hi:[1,0,1]
	v_and_b32_e32 v82, 0x7070707, v81
	v_and_b32_e32 v100, 0x7070707, v225
	v_pk_fma_f16 v96, v103, s59, v101 op_sel_hi:[1,0,1]
	v_perm_b32 v82, s2, v205, v82
	v_perm_b32 v100, s2, v205, v100
	v_and_or_b32 v82, v81, s4, v82
	v_and_or_b32 v81, v225, s4, v100
	v_perm_b32 v100, v81, v82, s5
	v_pk_fma_f16 v87, v102, s59, v87 op_sel_hi:[1,0,1]
	v_perm_b32 v101, v81, v82, s33
	v_perm_b32 v102, v81, v82, s0
	v_perm_b32 v81, v81, v82, s1
	v_pk_fma_f16 v82, v100, s59, v99 op_sel_hi:[1,0,1]
	v_readlane_b32 s60, v120, 8
	v_alignbit_b32 v224, v78, v78, 4
	v_pk_fma_f16 v98, v101, s59, v98 op_sel_hi:[1,0,1]
	v_pk_fma_f16 v97, v102, s59, v97 op_sel_hi:[1,0,1]
	v_pk_fma_f16 v81, v81, s59, v83 op_sel_hi:[1,0,1]
	v_and_b32_e32 v85, 0x7070707, v78
	v_and_b32_e32 v99, 0x7070707, v224
	v_perm_b32 v85, s2, v205, v85
	v_perm_b32 v99, s2, v205, v99
	v_and_or_b32 v85, v78, s4, v85
	v_and_or_b32 v78, v224, s4, v99
	v_perm_b32 v99, v78, v85, s5
	v_perm_b32 v100, v78, v85, s33
	v_perm_b32 v101, v78, v85, s0
	v_perm_b32 v78, v78, v85, s1
	v_pk_fma_f16 v85, v99, s60, v86 op_sel_hi:[1,0,1]
	v_pk_fma_f16 v86, v100, s60, v87 op_sel_hi:[1,0,1]
	v_pk_fma_f16 v87, v101, s60, v96 op_sel_hi:[1,0,1]
	v_alignbit_b32 v225, v79, v79, 4
	v_pk_fma_f16 v78, v78, s60, v80 op_sel_hi:[1,0,1]
	v_and_b32_e32 v80, 0x7070707, v79
	v_and_b32_e32 v96, 0x7070707, v225
	v_perm_b32 v80, s2, v205, v80
	v_perm_b32 v96, s2, v205, v96
	v_and_or_b32 v80, v79, s4, v80
	v_and_or_b32 v79, v225, s4, v96
	v_perm_b32 v96, v79, v80, s5
	v_perm_b32 v100, v79, v80, s0
	v_perm_b32 v99, v79, v80, s33
	v_perm_b32 v79, v79, v80, s1
	v_pk_fma_f16 v80, v96, s60, v82 op_sel_hi:[1,0,1]
	v_pk_fma_f16 v96, v100, s60, v97 op_sel_hi:[1,0,1]
	v_readlane_b32 s36, v120, 12
	v_alignbit_b32 v224, v76, v76, 4
	v_pk_fma_f16 v82, v99, s60, v98 op_sel_hi:[1,0,1]
	v_pk_fma_f16 v79, v79, s60, v81 op_sel_hi:[1,0,1]
	v_and_b32_e32 v83, 0x7070707, v76
	v_and_b32_e32 v97, 0x7070707, v224
	v_perm_b32 v83, s2, v205, v83
	v_perm_b32 v97, s2, v205, v97
	v_and_or_b32 v83, v76, s4, v83
	v_and_or_b32 v76, v224, s4, v97
	v_perm_b32 v97, v76, v83, s5
	v_perm_b32 v98, v76, v83, s33
	v_perm_b32 v99, v76, v83, s0
	v_perm_b32 v76, v76, v83, s1
	v_pk_fma_f16 v83, v97, s36, v85 op_sel_hi:[1,0,1]
	v_pk_fma_f16 v85, v98, s36, v86 op_sel_hi:[1,0,1]
	v_pk_fma_f16 v86, v99, s36, v87 op_sel_hi:[1,0,1]
	v_alignbit_b32 v225, v77, v77, 4
	v_pk_fma_f16 v76, v76, s36, v78 op_sel_hi:[1,0,1]
	v_and_b32_e32 v78, 0x7070707, v77
	v_and_b32_e32 v87, 0x7070707, v225
	v_perm_b32 v78, s2, v205, v78
	v_perm_b32 v87, s2, v205, v87
	v_and_or_b32 v78, v77, s4, v78
	v_and_or_b32 v77, v225, s4, v87
	v_perm_b32 v87, v77, v78, s5
	v_perm_b32 v97, v77, v78, s33
	v_perm_b32 v98, v77, v78, s0
	v_perm_b32 v77, v77, v78, s1
	v_pk_fma_f16 v78, v87, s36, v80 op_sel_hi:[1,0,1]
	v_readlane_b32 s59, v120, 16
	v_alignbit_b32 v224, v74, v74, 4
	v_pk_fma_f16 v80, v97, s36, v82 op_sel_hi:[1,0,1]
	v_pk_fma_f16 v82, v98, s36, v96 op_sel_hi:[1,0,1]
	v_pk_fma_f16 v77, v77, s36, v79 op_sel_hi:[1,0,1]
	v_and_b32_e32 v81, 0x7070707, v74
	v_and_b32_e32 v87, 0x7070707, v224
	v_perm_b32 v81, s2, v205, v81
	v_perm_b32 v87, s2, v205, v87
	v_and_or_b32 v81, v74, s4, v81
	v_and_or_b32 v74, v224, s4, v87
	v_perm_b32 v87, v74, v81, s5
	v_perm_b32 v96, v74, v81, s33
	v_perm_b32 v97, v74, v81, s0
	v_perm_b32 v74, v74, v81, s1
	v_pk_fma_f16 v81, v87, s59, v83 op_sel_hi:[1,0,1]
	v_pk_fma_f16 v83, v96, s59, v85 op_sel_hi:[1,0,1]
	v_pk_fma_f16 v85, v97, s59, v86 op_sel_hi:[1,0,1]
	v_alignbit_b32 v225, v75, v75, 4
	v_pk_fma_f16 v74, v74, s59, v76 op_sel_hi:[1,0,1]
	v_and_b32_e32 v76, 0x7070707, v75
	v_and_b32_e32 v86, 0x7070707, v225
	v_perm_b32 v76, s2, v205, v76
	v_perm_b32 v86, s2, v205, v86
	v_and_or_b32 v76, v75, s4, v76
	v_and_or_b32 v75, v225, s4, v86
	v_perm_b32 v86, v75, v76, s5
	v_perm_b32 v87, v75, v76, s33
	v_perm_b32 v96, v75, v76, s0
	v_perm_b32 v75, v75, v76, s1
	v_pk_fma_f16 v76, v86, s59, v78 op_sel_hi:[1,0,1]
	v_pk_fma_f16 v78, v87, s59, v80 op_sel_hi:[1,0,1]
	v_pk_fma_f16 v80, v96, s59, v82 op_sel_hi:[1,0,1]
	v_readlane_b32 s60, v120, 20
	v_alignbit_b32 v224, v70, v70, 4
	v_pk_fma_f16 v75, v75, s59, v77 op_sel_hi:[1,0,1]
	v_and_b32_e32 v79, 0x7070707, v70
	v_and_b32_e32 v82, 0x7070707, v224
	v_perm_b32 v79, s2, v205, v79
	v_perm_b32 v82, s2, v205, v82
	v_and_or_b32 v79, v70, s4, v79
	v_and_or_b32 v70, v224, s4, v82
	v_perm_b32 v82, v70, v79, s5
	v_perm_b32 v86, v70, v79, s33
	v_perm_b32 v87, v70, v79, s0
	v_perm_b32 v70, v70, v79, s1
	v_pk_fma_f16 v79, v82, s60, v81 op_sel_hi:[1,0,1]
	v_pk_fma_f16 v81, v86, s60, v83 op_sel_hi:[1,0,1]
	v_alignbit_b32 v225, v71, v71, 4
	v_pk_fma_f16 v70, v70, s60, v74 op_sel_hi:[1,0,1]
	v_and_b32_e32 v74, 0x7070707, v71
	v_and_b32_e32 v83, 0x7070707, v225
	v_pk_fma_f16 v82, v87, s60, v85 op_sel_hi:[1,0,1]
	v_perm_b32 v74, s2, v205, v74
	v_perm_b32 v83, s2, v205, v83
	v_and_or_b32 v74, v71, s4, v74
	v_and_or_b32 v71, v225, s4, v83
	v_perm_b32 v83, v71, v74, s5
	v_perm_b32 v85, v71, v74, s33
	v_perm_b32 v86, v71, v74, s0
	v_perm_b32 v71, v71, v74, s1
	v_pk_fma_f16 v74, v83, s60, v76 op_sel_hi:[1,0,1]
	v_pk_fma_f16 v76, v85, s60, v78 op_sel_hi:[1,0,1]
	v_pk_fma_f16 v78, v86, s60, v80 op_sel_hi:[1,0,1]
	v_readlane_b32 s36, v120, 24
	v_alignbit_b32 v224, v68, v68, 4
	v_pk_fma_f16 v71, v71, s60, v75 op_sel_hi:[1,0,1]
	v_and_b32_e32 v77, 0x7070707, v68
	v_and_b32_e32 v80, 0x7070707, v224
	v_perm_b32 v77, s2, v205, v77
	v_perm_b32 v80, s2, v205, v80
	v_and_or_b32 v77, v68, s4, v77
	v_and_or_b32 v68, v224, s4, v80
	v_perm_b32 v80, v68, v77, s5
	v_perm_b32 v83, v68, v77, s33
	v_perm_b32 v85, v68, v77, s0
	v_perm_b32 v68, v68, v77, s1
	v_pk_fma_f16 v77, v80, s36, v79 op_sel_hi:[1,0,1]
	v_pk_fma_f16 v79, v83, s36, v81 op_sel_hi:[1,0,1]
	v_alignbit_b32 v225, v69, v69, 4
	v_pk_fma_f16 v68, v68, s36, v70 op_sel_hi:[1,0,1]
	v_and_b32_e32 v70, 0x7070707, v69
	v_and_b32_e32 v81, 0x7070707, v225
	v_pk_fma_f16 v80, v85, s36, v82 op_sel_hi:[1,0,1]
	v_perm_b32 v70, s2, v205, v70
	v_perm_b32 v81, s2, v205, v81
	v_and_or_b32 v70, v69, s4, v70
	v_and_or_b32 v69, v225, s4, v81
	v_perm_b32 v81, v69, v70, s5
	v_perm_b32 v82, v69, v70, s33
	v_perm_b32 v83, v69, v70, s0
	v_perm_b32 v69, v69, v70, s1
	v_pk_fma_f16 v70, v81, s36, v74 op_sel_hi:[1,0,1]
	v_pk_fma_f16 v74, v82, s36, v76 op_sel_hi:[1,0,1]
	v_pk_fma_f16 v76, v83, s36, v78 op_sel_hi:[1,0,1]
	v_readlane_b32 s59, v120, 28
	v_alignbit_b32 v224, v64, v64, 4
	v_pk_fma_f16 v69, v69, s36, v71 op_sel_hi:[1,0,1]
	v_and_b32_e32 v75, 0x7070707, v64
	v_and_b32_e32 v78, 0x7070707, v224
	v_perm_b32 v75, s2, v205, v75
	v_perm_b32 v78, s2, v205, v78
	v_and_or_b32 v75, v64, s4, v75
	v_and_or_b32 v64, v224, s4, v78
	v_perm_b32 v78, v64, v75, s5
	v_perm_b32 v81, v64, v75, s33
	v_perm_b32 v82, v64, v75, s0
	v_perm_b32 v64, v64, v75, s1
	v_pk_fma_f16 v75, v78, s59, v77 op_sel_hi:[1,0,1]
	v_pk_fma_f16 v77, v81, s59, v79 op_sel_hi:[1,0,1]
	v_alignbit_b32 v225, v65, v65, 4
	v_pk_fma_f16 v64, v64, s59, v68 op_sel_hi:[1,0,1]
	v_and_b32_e32 v68, 0x7070707, v65
	v_and_b32_e32 v79, 0x7070707, v225
	v_pk_fma_f16 v78, v82, s59, v80 op_sel_hi:[1,0,1]
	v_perm_b32 v68, s2, v205, v68
	v_perm_b32 v79, s2, v205, v79
	v_and_or_b32 v68, v65, s4, v68
	v_and_or_b32 v65, v225, s4, v79
	v_perm_b32 v79, v65, v68, s5
	v_perm_b32 v80, v65, v68, s33
	v_perm_b32 v81, v65, v68, s0
	v_perm_b32 v65, v65, v68, s1
	v_pk_fma_f16 v68, v79, s59, v70 op_sel_hi:[1,0,1]
	v_pk_fma_f16 v70, v80, s59, v74 op_sel_hi:[1,0,1]
	v_pk_fma_f16 v74, v81, s59, v76 op_sel_hi:[1,0,1]
	v_readlane_b32 s60, v120, 32
	v_alignbit_b32 v224, v62, v62, 4
	v_pk_fma_f16 v65, v65, s59, v69 op_sel_hi:[1,0,1]
	v_and_b32_e32 v71, 0x7070707, v62
	v_and_b32_e32 v76, 0x7070707, v224
	v_perm_b32 v71, s2, v205, v71
	v_perm_b32 v76, s2, v205, v76
	v_and_or_b32 v71, v62, s4, v71
	v_and_or_b32 v62, v224, s4, v76
	v_perm_b32 v76, v62, v71, s5
	v_perm_b32 v79, v62, v71, s33
	v_perm_b32 v80, v62, v71, s0
	v_perm_b32 v62, v62, v71, s1
	v_pk_fma_f16 v71, v76, s60, v75 op_sel_hi:[1,0,1]
	v_pk_fma_f16 v75, v79, s60, v77 op_sel_hi:[1,0,1]
	v_alignbit_b32 v225, v63, v63, 4
	v_pk_fma_f16 v62, v62, s60, v64 op_sel_hi:[1,0,1]
	v_and_b32_e32 v64, 0x7070707, v63
	v_and_b32_e32 v77, 0x7070707, v225
	v_pk_fma_f16 v76, v80, s60, v78 op_sel_hi:[1,0,1]
	v_perm_b32 v64, s2, v205, v64
	v_perm_b32 v77, s2, v205, v77
	v_and_or_b32 v64, v63, s4, v64
	v_and_or_b32 v63, v225, s4, v77
	v_perm_b32 v77, v63, v64, s5
	v_perm_b32 v78, v63, v64, s33
	v_perm_b32 v79, v63, v64, s0
	v_perm_b32 v63, v63, v64, s1
	v_pk_fma_f16 v64, v77, s60, v68 op_sel_hi:[1,0,1]
	v_pk_fma_f16 v68, v78, s60, v70 op_sel_hi:[1,0,1]
	v_pk_fma_f16 v70, v79, s60, v74 op_sel_hi:[1,0,1]
	v_readlane_b32 s36, v120, 36
	v_alignbit_b32 v224, v66, v66, 4
	v_pk_fma_f16 v63, v63, s60, v65 op_sel_hi:[1,0,1]
	v_and_b32_e32 v69, 0x7070707, v66
	v_and_b32_e32 v74, 0x7070707, v224
	v_perm_b32 v69, s2, v205, v69
	v_perm_b32 v74, s2, v205, v74
	v_and_or_b32 v69, v66, s4, v69
	v_and_or_b32 v66, v224, s4, v74
	v_perm_b32 v74, v66, v69, s5
	v_perm_b32 v77, v66, v69, s33
	v_perm_b32 v78, v66, v69, s0
	v_perm_b32 v66, v66, v69, s1
	v_pk_fma_f16 v69, v74, s36, v71 op_sel_hi:[1,0,1]
	v_pk_fma_f16 v71, v77, s36, v75 op_sel_hi:[1,0,1]
	v_alignbit_b32 v225, v67, v67, 4
	v_pk_fma_f16 v62, v66, s36, v62 op_sel_hi:[1,0,1]
	v_and_b32_e32 v66, 0x7070707, v67
	v_and_b32_e32 v75, 0x7070707, v225
	v_pk_fma_f16 v74, v78, s36, v76 op_sel_hi:[1,0,1]
	v_perm_b32 v66, s2, v205, v66
	v_perm_b32 v75, s2, v205, v75
	v_and_or_b32 v66, v67, s4, v66
	v_and_or_b32 v67, v225, s4, v75
	v_perm_b32 v76, v67, v66, s33
	v_perm_b32 v77, v67, v66, s0
	v_perm_b32 v75, v67, v66, s5
	v_perm_b32 v66, v67, v66, s1
	v_pk_fma_f16 v67, v76, s36, v68 op_sel_hi:[1,0,1]
	v_pk_fma_f16 v68, v77, s36, v70 op_sel_hi:[1,0,1]
	v_readlane_b32 s59, v120, 40
	v_alignbit_b32 v224, v60, v60, 4
	v_pk_fma_f16 v64, v75, s36, v64 op_sel_hi:[1,0,1]
	v_pk_fma_f16 v63, v66, s36, v63 op_sel_hi:[1,0,1]
	v_and_b32_e32 v66, 0x7070707, v60
	v_and_b32_e32 v70, 0x7070707, v224
	v_perm_b32 v66, s2, v205, v66
	v_perm_b32 v70, s2, v205, v70
	v_and_or_b32 v66, v60, s4, v66
	v_and_or_b32 v60, v224, s4, v70
	v_perm_b32 v70, v60, v66, s5
	v_perm_b32 v75, v60, v66, s33
	v_perm_b32 v76, v60, v66, s0
	v_perm_b32 v60, v60, v66, s1
	v_pk_fma_f16 v66, v70, s59, v69 op_sel_hi:[1,0,1]
	v_pk_fma_f16 v69, v75, s59, v71 op_sel_hi:[1,0,1]
	v_alignbit_b32 v225, v61, v61, 4
	v_pk_fma_f16 v60, v60, s59, v62 op_sel_hi:[1,0,1]
	v_and_b32_e32 v62, 0x7070707, v61
	v_and_b32_e32 v71, 0x7070707, v225
	v_pk_fma_f16 v70, v76, s59, v74 op_sel_hi:[1,0,1]
	v_perm_b32 v62, s2, v205, v62
	v_perm_b32 v71, s2, v205, v71
	v_and_or_b32 v62, v61, s4, v62
	v_and_or_b32 v61, v225, s4, v71
	v_perm_b32 v71, v61, v62, s5
	v_perm_b32 v74, v61, v62, s33
	v_perm_b32 v75, v61, v62, s0
	v_perm_b32 v61, v61, v62, s1
	v_pk_fma_f16 v62, v71, s59, v64 op_sel_hi:[1,0,1]
	v_pk_fma_f16 v64, v74, s59, v67 op_sel_hi:[1,0,1]
	v_pk_fma_f16 v67, v75, s59, v68 op_sel_hi:[1,0,1]
	v_readlane_b32 s60, v120, 44
	v_alignbit_b32 v224, v58, v58, 4
	v_pk_fma_f16 v61, v61, s59, v63 op_sel_hi:[1,0,1]
	v_and_b32_e32 v65, 0x7070707, v58
	v_and_b32_e32 v68, 0x7070707, v224
	v_perm_b32 v65, s2, v205, v65
	v_perm_b32 v68, s2, v205, v68
	v_and_or_b32 v65, v58, s4, v65
	v_and_or_b32 v58, v224, s4, v68
	v_perm_b32 v68, v58, v65, s5
	v_perm_b32 v71, v58, v65, s33
	v_perm_b32 v74, v58, v65, s0
	v_perm_b32 v58, v58, v65, s1
	v_pk_fma_f16 v65, v68, s60, v66 op_sel_hi:[1,0,1]
	v_pk_fma_f16 v66, v71, s60, v69 op_sel_hi:[1,0,1]
	v_alignbit_b32 v225, v59, v59, 4
	v_pk_fma_f16 v58, v58, s60, v60 op_sel_hi:[1,0,1]
	v_and_b32_e32 v60, 0x7070707, v59
	v_and_b32_e32 v69, 0x7070707, v225
	v_pk_fma_f16 v68, v74, s60, v70 op_sel_hi:[1,0,1]
	v_perm_b32 v60, s2, v205, v60
	v_perm_b32 v69, s2, v205, v69
	v_and_or_b32 v60, v59, s4, v60
	v_and_or_b32 v59, v225, s4, v69
	v_perm_b32 v69, v59, v60, s5
	v_perm_b32 v70, v59, v60, s33
	v_perm_b32 v71, v59, v60, s0
	v_perm_b32 v59, v59, v60, s1
	v_pk_fma_f16 v60, v69, s60, v62 op_sel_hi:[1,0,1]
	v_pk_fma_f16 v62, v70, s60, v64 op_sel_hi:[1,0,1]
	v_pk_fma_f16 v64, v71, s60, v67 op_sel_hi:[1,0,1]
	v_readlane_b32 s36, v120, 48
	v_alignbit_b32 v224, v56, v56, 4
	v_pk_fma_f16 v59, v59, s60, v61 op_sel_hi:[1,0,1]
	v_and_b32_e32 v63, 0x7070707, v56
	v_and_b32_e32 v67, 0x7070707, v224
	v_perm_b32 v63, s2, v205, v63
	v_perm_b32 v67, s2, v205, v67
	v_and_or_b32 v63, v56, s4, v63
	v_and_or_b32 v56, v224, s4, v67
	v_perm_b32 v67, v56, v63, s5
	v_perm_b32 v69, v56, v63, s33
	v_perm_b32 v70, v56, v63, s0
	v_perm_b32 v56, v56, v63, s1
	v_pk_fma_f16 v63, v67, s36, v65 op_sel_hi:[1,0,1]
	v_alignbit_b32 v225, v57, v57, 4
	v_pk_fma_f16 v56, v56, s36, v58 op_sel_hi:[1,0,1]
	v_and_b32_e32 v58, 0x7070707, v57
	v_and_b32_e32 v67, 0x7070707, v225
	v_pk_fma_f16 v65, v69, s36, v66 op_sel_hi:[1,0,1]
	v_pk_fma_f16 v66, v70, s36, v68 op_sel_hi:[1,0,1]
	v_perm_b32 v58, s2, v205, v58
	v_perm_b32 v67, s2, v205, v67
	v_and_or_b32 v58, v57, s4, v58
	v_and_or_b32 v57, v225, s4, v67
	v_perm_b32 v67, v57, v58, s5
	v_perm_b32 v68, v57, v58, s33
	v_perm_b32 v69, v57, v58, s0
	v_perm_b32 v57, v57, v58, s1
	v_pk_fma_f16 v58, v67, s36, v60 op_sel_hi:[1,0,1]
	v_pk_fma_f16 v60, v68, s36, v62 op_sel_hi:[1,0,1]
	v_pk_fma_f16 v62, v69, s36, v64 op_sel_hi:[1,0,1]
	v_readlane_b32 s59, v120, 52
	v_alignbit_b32 v224, v54, v54, 4
	v_pk_fma_f16 v57, v57, s36, v59 op_sel_hi:[1,0,1]
	v_and_b32_e32 v61, 0x7070707, v54
	v_and_b32_e32 v64, 0x7070707, v224
	v_perm_b32 v61, s2, v205, v61
	v_perm_b32 v64, s2, v205, v64
	v_and_or_b32 v61, v54, s4, v61
	v_and_or_b32 v54, v224, s4, v64
	v_perm_b32 v64, v54, v61, s5
	v_perm_b32 v67, v54, v61, s33
	v_perm_b32 v68, v54, v61, s0
	v_perm_b32 v54, v54, v61, s1
	v_pk_fma_f16 v61, v64, s59, v63 op_sel_hi:[1,0,1]
	v_pk_fma_f16 v63, v67, s59, v65 op_sel_hi:[1,0,1]
	v_alignbit_b32 v225, v55, v55, 4
	v_pk_fma_f16 v54, v54, s59, v56 op_sel_hi:[1,0,1]
	v_and_b32_e32 v56, 0x7070707, v55
	v_and_b32_e32 v65, 0x7070707, v225
	v_pk_fma_f16 v64, v68, s59, v66 op_sel_hi:[1,0,1]
	v_perm_b32 v56, s2, v205, v56
	v_perm_b32 v65, s2, v205, v65
	v_and_or_b32 v56, v55, s4, v56
	v_and_or_b32 v55, v225, s4, v65
	v_perm_b32 v65, v55, v56, s5
	v_perm_b32 v66, v55, v56, s33
	v_perm_b32 v67, v55, v56, s0
	v_perm_b32 v55, v55, v56, s1
	v_pk_fma_f16 v56, v65, s59, v58 op_sel_hi:[1,0,1]
	v_pk_fma_f16 v58, v66, s59, v60 op_sel_hi:[1,0,1]
	v_pk_fma_f16 v60, v67, s59, v62 op_sel_hi:[1,0,1]
	v_readlane_b32 s60, v120, 56
	v_alignbit_b32 v224, v52, v52, 4
	v_pk_fma_f16 v55, v55, s59, v57 op_sel_hi:[1,0,1]
	v_and_b32_e32 v59, 0x7070707, v52
	v_and_b32_e32 v62, 0x7070707, v224
	v_perm_b32 v59, s2, v205, v59
	v_perm_b32 v62, s2, v205, v62
	v_and_or_b32 v59, v52, s4, v59
	v_and_or_b32 v52, v224, s4, v62
	v_perm_b32 v62, v52, v59, s5
	v_perm_b32 v65, v52, v59, s33
	v_perm_b32 v66, v52, v59, s0
	v_perm_b32 v52, v52, v59, s1
	v_pk_fma_f16 v59, v62, s60, v61 op_sel_hi:[1,0,1]
	v_pk_fma_f16 v61, v65, s60, v63 op_sel_hi:[1,0,1]
	v_alignbit_b32 v225, v53, v53, 4
	v_pk_fma_f16 v52, v52, s60, v54 op_sel_hi:[1,0,1]
	v_and_b32_e32 v54, 0x7070707, v53
	v_and_b32_e32 v63, 0x7070707, v225
	v_pk_fma_f16 v62, v66, s60, v64 op_sel_hi:[1,0,1]
	v_perm_b32 v54, s2, v205, v54
	v_perm_b32 v63, s2, v205, v63
	v_and_or_b32 v54, v53, s4, v54
	v_and_or_b32 v53, v225, s4, v63
	v_perm_b32 v63, v53, v54, s5
	v_perm_b32 v64, v53, v54, s33
	v_perm_b32 v65, v53, v54, s0
	v_perm_b32 v53, v53, v54, s1
	v_pk_fma_f16 v54, v63, s60, v56 op_sel_hi:[1,0,1]
	v_pk_fma_f16 v56, v64, s60, v58 op_sel_hi:[1,0,1]
	v_pk_fma_f16 v58, v65, s60, v60 op_sel_hi:[1,0,1]
	v_readlane_b32 s36, v120, 60
	v_alignbit_b32 v224, v36, v36, 4
	v_pk_fma_f16 v53, v53, s60, v55 op_sel_hi:[1,0,1]
	v_and_b32_e32 v57, 0x7070707, v36
	v_and_b32_e32 v60, 0x7070707, v224
	v_perm_b32 v57, s2, v205, v57
	v_perm_b32 v60, s2, v205, v60
	v_and_or_b32 v57, v36, s4, v57
	v_and_or_b32 v36, v224, s4, v60
	v_perm_b32 v60, v36, v57, s5
	v_perm_b32 v63, v36, v57, s33
	v_perm_b32 v64, v36, v57, s0
	v_perm_b32 v36, v36, v57, s1
	v_pk_fma_f16 v100, v36, s36, v52 op_sel_hi:[1,0,1]
	v_alignbit_b32 v225, v37, v37, 4
	v_and_b32_e32 v36, 0x7070707, v37
	v_and_b32_e32 v52, 0x7070707, v225
	v_perm_b32 v36, s2, v205, v36
	v_perm_b32 v52, s2, v205, v52
	v_and_or_b32 v36, v37, s4, v36
	v_and_or_b32 v37, v225, s4, v52
	v_pk_fma_f16 v103, v60, s36, v59 op_sel_hi:[1,0,1]
	v_perm_b32 v52, v37, v36, s5
	v_perm_b32 v57, v37, v36, s33
	v_perm_b32 v59, v37, v36, s0
	v_perm_b32 v36, v37, v36, s1
	v_pk_fma_f16 v96, v36, s36, v53 op_sel_hi:[1,0,1]
	s_add_u32 s66, s12, s64
	s_addc_u32 s67, s13, s65
	global_load_dwordx2 v[82:83], v121, s[66:67]
	s_add_u32 s66, s14, s64
	s_addc_u32 s67, s15, s65
	global_load_dwordx2 v[80:81], v121, s[66:67]
	s_add_u32 s66, s38, s62
	s_addc_u32 s67, s39, s63
	global_load_dwordx2 v[48:49], v121, s[66:67]
	s_add_u32 s66, s16, s64
	s_addc_u32 s67, s17, s65
	global_load_dwordx2 v[78:79], v121, s[66:67]
	s_add_u32 s66, s50, s62
	s_addc_u32 s67, s51, s63
	global_load_dwordx2 v[46:47], v121, s[66:67]
	s_add_u32 s66, s18, s64
	s_addc_u32 s67, s19, s65
	global_load_dwordx2 v[76:77], v121, s[66:67]
	s_add_u32 s66, s52, s62
	s_addc_u32 s67, s53, s63
	global_load_dwordx2 v[44:45], v121, s[66:67]
	s_add_u32 s66, s20, s64
	s_addc_u32 s67, s21, s65
	global_load_dwordx2 v[74:75], v121, s[66:67]
	s_add_u32 s66, s54, s62
	s_addc_u32 s67, s55, s63
	global_load_dwordx2 v[42:43], v121, s[66:67]
	s_add_u32 s66, s22, s64
	s_addc_u32 s67, s23, s65
	global_load_dwordx2 v[70:71], v121, s[66:67]
	s_add_u32 s66, s56, s62
	s_addc_u32 s67, s57, s63
	global_load_dwordx2 v[40:41], v121, s[66:67]
	v_pk_fma_f16 v101, v64, s36, v62 op_sel_hi:[1,0,1]
	s_add_u32 s66, s24, s64
	s_addc_u32 s67, s25, s65
	global_load_dwordx2 v[68:69], v121, s[66:67]
	s_add_u32 s66, s26, s64
	s_addc_u32 s67, s27, s65
	global_load_dwordx2 v[64:65], v121, s[66:67]
	v_pk_fma_f16 v102, v63, s36, v61 op_sel_hi:[1,0,1]
	s_add_u32 s66, s28, s64
	s_addc_u32 s67, s29, s65
	global_load_dwordx2 v[62:63], v121, s[66:67]
	s_add_u32 s66, s30, s64
	s_addc_u32 s67, s31, s65
	global_load_dwordx2 v[66:67], v121, s[66:67]
	s_add_u32 s66, s34, s64
	s_addc_u32 s67, s35, s65
	global_load_dwordx2 v[60:61], v121, s[66:67]
	v_pk_fma_f16 v97, v59, s36, v58 op_sel_hi:[1,0,1]
	s_add_u32 s66, s38, s64
	s_addc_u32 s67, s39, s65
	global_load_dwordx2 v[58:59], v121, s[66:67]
	v_pk_fma_f16 v98, v57, s36, v56 op_sel_hi:[1,0,1]
	s_add_u32 s66, s50, s64
	s_addc_u32 s67, s51, s65
	global_load_dwordx2 v[56:57], v121, s[66:67]
	v_pk_fma_f16 v99, v52, s36, v54 op_sel_hi:[1,0,1]
	s_add_u32 s66, s52, s64
	s_addc_u32 s67, s53, s65
	global_load_dwordx2 v[54:55], v121, s[66:67]
	s_add_u32 s66, s54, s64
	s_addc_u32 s67, s55, s65
	global_load_dwordx2 v[52:53], v121, s[66:67]
	s_add_u32 s66, s12, s62
	s_addc_u32 s67, s13, s63
	global_load_dwordx2 v[8:9], v121, s[66:67]
	s_add_u32 s66, s14, s62
	s_addc_u32 s67, s15, s63
	global_load_dwordx2 v[10:11], v121, s[66:67]
	s_nop 0
	s_add_u32 s66, s16, s62
	s_addc_u32 s67, s17, s63
	global_load_dwordx2 v[12:13], v121, s[66:67]
	s_nop 0
	s_add_u32 s66, s18, s62
	s_addc_u32 s67, s19, s63
	global_load_dwordx2 v[14:15], v121, s[66:67]
	s_nop 0
	s_add_u32 s66, s20, s62
	s_addc_u32 s67, s21, s63
	global_load_dwordx2 v[16:17], v121, s[66:67]
	s_nop 0
	s_add_u32 s66, s22, s62
	s_addc_u32 s67, s23, s63
	global_load_dwordx2 v[18:19], v121, s[66:67]
	s_nop 0
	s_add_u32 s66, s24, s62
	s_addc_u32 s67, s25, s63
	global_load_dwordx2 v[20:21], v121, s[66:67]
	s_nop 0
	s_add_u32 s66, s26, s62
	s_addc_u32 s67, s27, s63
	global_load_dwordx2 v[22:23], v121, s[66:67]
	s_nop 0
	s_add_u32 s66, s56, s64
	s_addc_u32 s67, s57, s65
	global_load_dwordx2 v[36:37], v121, s[66:67]
	s_cmpk_eq_i32 s58, 0x90
	s_cbranch_scc0 .LBB0_763
	v_lshlrev_b64 v[0:1], 2, v[2:3]
	v_lshl_add_u64 v[2:3], v[28:29], 0, v[0:1]
	v_mov_b32_e32 v104, v208
	v_mov_b32_e32 v105, v209
	v_mov_b32_e32 v106, v210
	v_mov_b32_e32 v107, v211
	v_mov_b32_e32 v108, v212
	v_mov_b32_e32 v109, v213
	v_mov_b32_e32 v110, v214
	v_mov_b32_e32 v111, v215
	v_mov_b32_e32 v86, v216
	v_mov_b32_e32 v87, v217
	v_mov_b32_e32 v88, v218
	v_mov_b32_e32 v89, v219
	v_mov_b32_e32 v112, v220
	v_mov_b32_e32 v113, v221
	v_mov_b32_e32 v114, v222
	v_mov_b32_e32 v115, v223
	v_lshl_add_u64 v[72:73], v[32:33], 0, v[0:1]
	v_cvt_f32_f16_sdwa v1, v103 dst_sel:DWORD dst_unused:UNUSED_PAD src0_sel:WORD_1
	v_cvt_f32_f16_e32 v0, v103
	v_cvt_f32_f16_sdwa v91, v102 dst_sel:DWORD dst_unused:UNUSED_PAD src0_sel:WORD_1
	v_cvt_f32_f16_e32 v90, v102
	v_cvt_f32_f16_sdwa v103, v101 dst_sel:DWORD dst_unused:UNUSED_PAD src0_sel:WORD_1
	v_cvt_f32_f16_e32 v102, v101
	v_cvt_f32_f16_sdwa v101, v100 dst_sel:DWORD dst_unused:UNUSED_PAD src0_sel:WORD_1
	v_cvt_f32_f16_e32 v100, v100
	s_mov_b32 s18, 0x800000
	v_readlane_b32 s12, v255, 5
	v_readlane_b32 s13, v255, 6
	v_pk_add_f32 v[86:87], v[86:87], v[102:103]
	v_pk_add_f32 v[84:85], v[112:113], v[0:1]
	v_mov_b32_e32 v102, v85
	v_mov_b32_e32 v103, v87
	v_pk_add_f32 v[90:91], v[114:115], v[90:91]
	v_pk_add_f32 v[88:89], v[88:89], v[100:101]
	v_mov_b32_e32 v100, v84
	v_mov_b32_e32 v101, v86
	v_pk_mul_f32 v[102:103], v[102:103], v[102:103]
	v_mov_b32_e32 v112, v91
	v_pk_fma_f32 v[100:101], v[100:101], v[100:101], v[102:103]
	v_mov_b32_e32 v102, v90
	v_mov_b32_e32 v103, v88
	v_pk_fma_f32 v[100:101], v[102:103], v[102:103], v[100:101]
	v_cvt_f32_f16_sdwa v103, v99 dst_sel:DWORD dst_unused:UNUSED_PAD src0_sel:WORD_1
	v_cvt_f32_f16_e32 v102, v99
	v_cvt_f32_f16_sdwa v99, v98 dst_sel:DWORD dst_unused:UNUSED_PAD src0_sel:WORD_1
	v_cvt_f32_f16_e32 v98, v98
	v_mov_b32_e32 v113, v89
	v_pk_add_f32 v[102:103], v[108:109], v[102:103]
	v_cvt_f32_f16_sdwa v109, v97 dst_sel:DWORD dst_unused:UNUSED_PAD src0_sel:WORD_1
	v_cvt_f32_f16_e32 v108, v97
	v_cvt_f32_f16_sdwa v97, v96 dst_sel:DWORD dst_unused:UNUSED_PAD src0_sel:WORD_1
	v_cvt_f32_f16_e32 v96, v96
	v_pk_add_f32 v[98:99], v[110:111], v[98:99]
	v_pk_add_f32 v[104:105], v[104:105], v[108:109]
	v_mov_b32_e32 v108, v103
	v_mov_b32_e32 v109, v105
	v_pk_add_f32 v[96:97], v[106:107], v[96:97]
	v_mov_b32_e32 v106, v102
	v_mov_b32_e32 v107, v104
	v_pk_mul_f32 v[108:109], v[108:109], v[108:109]
	v_pk_fma_f32 v[100:101], v[112:113], v[112:113], v[100:101]
	v_pk_fma_f32 v[106:107], v[106:107], v[106:107], v[108:109]
	v_mov_b32_e32 v108, v98
	v_mov_b32_e32 v109, v96
	v_mov_b32_e32 v110, v99
	v_mov_b32_e32 v111, v97
	v_pk_fma_f32 v[106:107], v[108:109], v[108:109], v[106:107]
	v_add_f32_e32 v95, v100, v101
	v_pk_fma_f32 v[106:107], v[110:111], v[110:111], v[106:107]
	v_lshl_add_u64 v[34:35], v[34:35], 0, s[12:13]
	v_add_f32_e32 v95, v95, v106
	v_add_f32_e32 v95, v95, v107
	v_mov_b32_e32 v100, v95
	s_nop 1
	v_permlane32_swap_b32 v100, v95
	s_waitcnt lgkmcnt(0)
	v_add_f32_e32 v95, v95, v100
	v_mov_b32_e32 v100, v95
	s_nop 1
	v_permlane16_swap_b32 v100, v95
	s_waitcnt lgkmcnt(0)
	v_add_f32_e32 v95, v95, v100
	s_nop 1
	v_mov_b32_dpp v100, v95 row_ror:8 row_mask:0xf bank_mask:0xf
	s_waitcnt lgkmcnt(0)
	v_add_f32_e32 v95, v95, v100
	s_nop 1
	v_mov_b32_dpp v100, v95 row_half_mirror row_mask:0xf bank_mask:0xf
	s_nop 1
	v_mov_b32_dpp v100, v100 quad_perm:[3,2,1,0] row_mask:0xf bank_mask:0xf
	s_waitcnt lgkmcnt(0)
	v_add_f32_e32 v95, v95, v100
	s_nop 1
	v_mov_b32_dpp v100, v95 quad_perm:[2,3,0,1] row_mask:0xf bank_mask:0xf
	s_waitcnt lgkmcnt(0)
	v_add_f32_e32 v95, v95, v100
	s_nop 1
	v_mov_b32_dpp v100, v95 quad_perm:[1,0,3,2] row_mask:0xf bank_mask:0xf
	s_waitcnt lgkmcnt(0)
	v_add_f32_e32 v95, v95, v100
	v_fmamk_f32 v95, v95, 0x3a800000, v191
	v_cmp_gt_f32_e32 vcc, s18, v95
	v_mul_f32_e32 v100, 0x4b800000, v95
	s_nop 0
	v_cndmask_b32_e32 v95, v95, v100, vcc
	v_rsq_f32_e32 v95, v95
	s_nop 0
	v_mul_f32_e32 v100, 0x45800000, v95
	v_cndmask_b32_e32 v100, v95, v100, vcc
	v_pk_mul_f32 v[84:85], v[84:85], v[100:101] op_sel_hi:[1,0]
	v_pk_mul_f32 v[0:1], v[124:125], v[84:85]
	v_pk_mul_f32 v[84:85], v[90:91], v[100:101] op_sel_hi:[1,0]
	s_nop 0
	v_pk_mul_f32 v[2:3], v[126:127], v[84:85]
	global_store_dwordx4 v[72:73], v[0:3], off
	s_nop 1
	v_pk_mul_f32 v[84:85], v[86:87], v[100:101] op_sel_hi:[1,0]
	v_pk_mul_f32 v[0:1], v[128:129], v[84:85]
	v_pk_mul_f32 v[84:85], v[88:89], v[100:101] op_sel_hi:[1,0]
	s_nop 0
	v_pk_mul_f32 v[2:3], v[130:131], v[84:85]
	global_store_dwordx4 v[72:73], v[0:3], off offset:16
	s_nop 1
	v_pk_mul_f32 v[84:85], v[102:103], v[100:101] op_sel_hi:[1,0]
	v_pk_mul_f32 v[0:1], v[84:85], v[132:133]
	v_pk_mul_f32 v[84:85], v[98:99], v[100:101] op_sel_hi:[1,0]
	s_nop 0
	v_pk_mul_f32 v[2:3], v[84:85], v[134:135]
	global_store_dwordx4 v[72:73], v[0:3], off offset:32
	s_nop 1
	v_pk_mul_f32 v[84:85], v[104:105], v[100:101] op_sel_hi:[1,0]
	v_pk_mul_f32 v[0:1], v[84:85], v[136:137]
	v_pk_mul_f32 v[84:85], v[96:97], v[100:101] op_sel_hi:[1,0]
	s_nop 0
	v_pk_mul_f32 v[2:3], v[84:85], v[138:139]
	global_store_dwordx4 v[72:73], v[0:3], off offset:48
	s_nop 1
	v_mov_b32_e32 v0, v94
	s_andn2_b64 exec, exec, s[10:11]
	s_cbranch_execnz .LBB0_762

.LBB0_770:
	s_cmpk_eq_i32 s56, 0x80
	s_cselect_b64 s[10:11], -1, 0
	ds_bpermute_b32 v6, v97, v96
	s_and_b64 vcc, s[10:11], s[48:49]
	v_cndmask_b32_e32 v94, v0, v98, vcc
	v_ashrrev_i32_e32 v95, 31, v94
	s_and_b32 s10, s56, 0x70
	v_lshlrev_b64 v[94:95], 9, v[94:95]
	v_lshl_add_u64 v[94:95], s[94:95], 0, v[94:95]
	s_lshl_b32 s36, s10, 2
	s_waitcnt lgkmcnt(0)
	v_ashrrev_i32_e32 v7, 31, v6
	v_lshl_add_u64 v[94:95], v[94:95], 0, s[36:37]
	v_lshl_add_u64 v[6:7], v[6:7], 3, s[88:89]
	v_lshl_add_u64 v[94:95], v[94:95], 0, v[144:145]
	global_load_dwordx2 v[6:7], v[6:7], off
	s_nop 0
	global_load_dword v8, v[4:5], off
	global_load_dword v96, v[94:95], off
	s_waitcnt vmcnt(33)
	v_dot8_i32_i4 v9, v20, v1, 0
	v_dot8_i32_i4 v94, v20, v10, 0
	v_dot8_i32_i4 v9, v21, v11, v9
	v_dot8_i32_i4 v94, v21, v12, v94
	v_dot8_i32_i4 v20, v22, v1, 0
	v_dot8_i32_i4 v21, v22, v10, 0
	v_dot8_i32_i4 v20, v23, v11, v20
	v_dot8_i32_i4 v21, v23, v12, v21
	v_lshl_add_u32 v9, v9, 4, v94
	s_add_i32 s56, s56, 16
	s_nop 0
	v_lshl_add_u32 v94, v20, 4, v21
	s_waitcnt vmcnt(32)
	v_dot8_i32_i4 v20, v24, v1, 0
	v_dot8_i32_i4 v21, v24, v10, 0
	v_dot8_i32_i4 v20, v25, v11, v20
	v_dot8_i32_i4 v21, v25, v12, v21
	v_lshl_add_u64 v[4:5], v[4:5], 0, 64
	s_waitcnt vmcnt(2)
	v_mul_f32_e32 v7, v13, v7
	v_lshl_add_u32 v95, v20, 4, v21
	v_dot8_i32_i4 v20, v26, v1, 0
	v_dot8_i32_i4 v21, v26, v10, 0
	v_dot8_i32_i4 v20, v27, v11, v20
	v_dot8_i32_i4 v21, v27, v12, v21
	s_waitcnt vmcnt(0)
	v_readlane_b32 s10, v96, 0
	s_ashr_i32 s11, s10, 31
	v_readlane_b32 s12, v96, 1
	v_lshl_add_u32 v106, v20, 4, v21
	v_dot8_i32_i4 v20, v28, v1, 0
	v_dot8_i32_i4 v21, v28, v10, 0
	v_dot8_i32_i4 v20, v29, v11, v20
	v_dot8_i32_i4 v21, v29, v12, v21
	s_lshl_b64 s[10:11], s[10:11], 9
	s_ashr_i32 s13, s12, 31
	v_readlane_b32 s14, v96, 2
	v_lshl_add_u32 v107, v20, 4, v21
	v_dot8_i32_i4 v20, v30, v1, 0
	v_dot8_i32_i4 v21, v30, v10, 0
	v_dot8_i32_i4 v20, v31, v11, v20
	v_dot8_i32_i4 v21, v31, v12, v21
	s_lshl_b64 s[12:13], s[12:13], 9
	s_ashr_i32 s15, s14, 31
	v_readlane_b32 s16, v96, 3
	v_lshl_add_u32 v108, v20, 4, v21
	v_dot8_i32_i4 v20, v32, v1, 0
	v_dot8_i32_i4 v21, v32, v10, 0
	v_dot8_i32_i4 v20, v33, v11, v20
	v_dot8_i32_i4 v21, v33, v12, v21
	s_lshl_b64 s[14:15], s[14:15], 9
	s_ashr_i32 s17, s16, 31
	s_nop 0
	v_lshl_add_u32 v109, v20, 4, v21
	v_dot8_i32_i4 v20, v34, v1, 0
	v_dot8_i32_i4 v21, v34, v10, 0
	v_dot8_i32_i4 v20, v35, v11, v20
	v_dot8_i32_i4 v21, v35, v12, v21
	v_readlane_b32 s18, v96, 4
	s_add_u32 s66, s12, s62
	s_addc_u32 s67, s13, s63
	global_load_dwordx2 v[22:23], v121, s[66:67]
	v_lshl_add_u32 v110, v20, 4, v21
	v_dot8_i32_i4 v20, v36, v1, 0
	v_dot8_i32_i4 v21, v36, v10, 0
	v_dot8_i32_i4 v20, v37, v11, v20
	v_dot8_i32_i4 v21, v37, v12, v21
	s_lshl_b64 s[16:17], s[16:17], 9
	s_ashr_i32 s19, s18, 31
	v_readlane_b32 s20, v96, 5
	v_lshl_add_u32 v111, v20, 4, v21
	v_dot8_i32_i4 v20, v38, v1, 0
	v_dot8_i32_i4 v21, v38, v10, 0
	v_dot8_i32_i4 v20, v39, v11, v20
	v_dot8_i32_i4 v21, v39, v12, v21
	s_setprio 2
	v_permlane32_swap_b32 v9, v111
	s_nop 1
	v_lshl_add_u32 v112, v20, 4, v21
	v_dot8_i32_i4 v20, v40, v1, 0
	v_dot8_i32_i4 v21, v40, v10, 0
	v_dot8_i32_i4 v20, v41, v11, v20
	v_dot8_i32_i4 v21, v41, v12, v21
	s_waitcnt lgkmcnt(0)
	v_add_u32_e32 v9, v9, v111
	v_permlane32_swap_b32 v94, v112
	v_lshl_add_u32 v113, v20, 4, v21
	v_dot8_i32_i4 v20, v60, v1, 0
	v_dot8_i32_i4 v21, v60, v10, 0
	v_dot8_i32_i4 v20, v61, v11, v20
	v_dot8_i32_i4 v21, v61, v12, v21
	s_waitcnt lgkmcnt(0)
	v_add_u32_e32 v94, v94, v112
	v_permlane32_swap_b32 v95, v113
	v_lshl_add_u32 v114, v20, 4, v21
	v_dot8_i32_i4 v20, v58, v1, 0
	v_dot8_i32_i4 v21, v58, v10, 0
	v_dot8_i32_i4 v20, v59, v11, v20
	v_dot8_i32_i4 v21, v59, v12, v21
	s_waitcnt lgkmcnt(0)
	v_add_u32_e32 v95, v95, v113
	v_permlane32_swap_b32 v106, v114
	v_lshl_add_u32 v115, v20, 4, v21
	v_dot8_i32_i4 v20, v56, v1, 0
	v_dot8_i32_i4 v21, v56, v10, 0
	v_dot8_i32_i4 v20, v57, v11, v20
	v_dot8_i32_i4 v21, v57, v12, v21
	s_waitcnt lgkmcnt(0)
	v_add_u32_e32 v106, v106, v114
	v_permlane32_swap_b32 v107, v115
	v_lshl_add_u32 v116, v20, 4, v21
	v_dot8_i32_i4 v20, v54, v1, 0
	v_dot8_i32_i4 v21, v54, v10, 0
	v_dot8_i32_i4 v20, v55, v11, v20
	v_dot8_i32_i4 v21, v55, v12, v21
	s_waitcnt lgkmcnt(0)
	v_add_u32_e32 v107, v107, v115
	v_permlane32_swap_b32 v108, v116
	v_lshl_add_u32 v117, v20, 4, v21
	v_dot8_i32_i4 v20, v52, v1, 0
	v_dot8_i32_i4 v21, v52, v10, 0
	v_dot8_i32_i4 v20, v53, v11, v20
	v_dot8_i32_i4 v21, v53, v12, v21
	s_waitcnt lgkmcnt(0)
	v_add_u32_e32 v108, v108, v116
	v_permlane32_swap_b32 v109, v117
	v_lshl_add_u32 v118, v20, 4, v21
	s_waitcnt lgkmcnt(0)
	v_add_u32_e32 v109, v109, v117
	v_permlane32_swap_b32 v110, v118
	s_add_u32 s66, s10, s62
	s_addc_u32 s67, s11, s63
	global_load_dwordx2 v[20:21], v121, s[66:67]
	s_add_u32 s66, s14, s62
	s_addc_u32 s67, s15, s63
	global_load_dwordx2 v[24:25], v121, s[66:67]
	s_waitcnt lgkmcnt(0)
	v_add_u32_e32 v110, v110, v118
	v_permlane16_swap_b32 v9, v107
	s_lshl_b64 s[18:19], s[18:19], 9
	s_ashr_i32 s21, s20, 31
	v_readlane_b32 s22, v96, 6
	s_add_u32 s66, s16, s62
	s_addc_u32 s67, s17, s63
	global_load_dwordx2 v[26:27], v121, s[66:67]
	s_waitcnt lgkmcnt(0)
	v_add_u32_e32 v9, v9, v107
	v_permlane16_swap_b32 v94, v108
	s_lshl_b64 s[20:21], s[20:21], 9
	s_ashr_i32 s23, s22, 31
	s_waitcnt lgkmcnt(0)
	v_add_u32_e32 v94, v94, v108
	v_permlane16_swap_b32 v95, v109
	v_readlane_b32 s24, v96, 7
	s_add_u32 s66, s18, s62
	s_addc_u32 s67, s19, s63
	global_load_dwordx2 v[28:29], v121, s[66:67]
	s_waitcnt lgkmcnt(0)
	v_add_u32_e32 v95, v95, v109
	v_permlane16_swap_b32 v106, v110
	s_lshl_b64 s[22:23], s[22:23], 9
	s_ashr_i32 s25, s24, 31
	v_readlane_b32 s26, v96, 8
	s_waitcnt lgkmcnt(0)
	v_add_u32_e32 v106, v106, v110
	v_cndmask_b32_e64 v107, v9, v95, s[44:45]
	v_cndmask_b32_e64 v9, v95, v9, s[44:45]
	s_nop 0
	s_add_u32 s66, s20, s62
	s_addc_u32 s67, s21, s63
	global_load_dwordx2 v[30:31], v121, s[66:67]
	s_lshl_b64 s[24:25], s[24:25], 9
	s_ashr_i32 s27, s26, 31
	s_waitcnt lgkmcnt(0)
	v_add_u32_dpp v9, v107, v9 row_ror:8 row_mask:0xf bank_mask:0xf
	v_cndmask_b32_e64 v95, v94, v106, s[44:45]
	s_nop 1
	v_cndmask_b32_e64 v94, v106, v94, s[44:45]
	v_readlane_b32 s28, v96, 9
	s_add_u32 s66, s22, s62
	s_addc_u32 s67, s23, s63
	global_load_dwordx2 v[32:33], v121, s[66:67]
	s_waitcnt lgkmcnt(0)
	v_add_u32_dpp v94, v95, v94 row_ror:8 row_mask:0xf bank_mask:0xf
	v_cndmask_b32_e64 v95, v9, v94, s[46:47]
	v_cndmask_b32_e64 v9, v94, v9, s[46:47]
	s_nop 0
	v_mov_b32_dpp v94, v95 row_half_mirror row_mask:0xf bank_mask:0xf
	s_nop 1
	s_lshl_b64 s[26:27], s[26:27], 9
	s_ashr_i32 s29, s28, 31
	v_readlane_b32 s30, v96, 10
	s_add_u32 s66, s24, s62
	s_addc_u32 s67, s25, s63
	global_load_dwordx2 v[34:35], v121, s[66:67]
	s_waitcnt lgkmcnt(0)
	v_add_u32_dpp v9, v94, v9 quad_perm:[3,2,1,0] row_mask:0xf bank_mask:0xf
	s_nop 1
	s_lshl_b64 s[28:29], s[28:29], 9
	s_ashr_i32 s31, s30, 31
	v_readlane_b32 s34, v96, 11
	s_waitcnt lgkmcnt(0)
	v_add_u32_dpp v9, v9, v9 quad_perm:[2,3,0,1] row_mask:0xf bank_mask:0xf
	s_nop 1
	s_add_u32 s66, s26, s62
	s_addc_u32 s67, s27, s63
	global_load_dwordx2 v[36:37], v121, s[66:67]
	s_lshl_b64 s[30:31], s[30:31], 9
	s_ashr_i32 s35, s34, 31
	s_waitcnt lgkmcnt(0)
	v_add_u32_dpp v9, v9, v9 quad_perm:[1,0,3,2] row_mask:0xf bank_mask:0xf
	v_cvt_f32_i32_e32 v9, v9
	v_add_f32_e32 v9, v14, v9
	v_mul_f32_e32 v7, v7, v9
	v_mul_f32_e32 v9, 0x3d372713, v7
	v_mul_f32_e32 v9, v7, v9
	v_fma_f32 v9, v7, v9, v7
	v_mul_f32_e32 v9, 0x3fcc422a, v9
	v_mul_f32_e32 v9, 0xbfb8aa3b, v9
	v_exp_f32_e32 v9, v9
	v_readlane_b32 s38, v96, 12
	s_add_u32 s66, s28, s62
	s_addc_u32 s67, s29, s63
	global_load_dwordx2 v[38:39], v121, s[66:67]
	v_add_f32_e32 v9, 1.0, v9
	v_rcp_f32_e32 v9, v9
	s_lshl_b64 s[34:35], s[34:35], 9
	s_ashr_i32 s39, s38, 31
	v_pk_mul_f32 v[6:7], v[6:7], v[8:9]
	v_alignbit_b32 v224, v92, v92, 4
	v_pk_mul_f32 v[6:7], v[6:7], v[6:7] op_sel:[0,1] op_sel_hi:[1,0]
	v_cvt_f16_f32_e32 v120, v6
	s_setprio 0
	v_and_b32_e32 v8, 0x7070707, v92
	v_readlane_b32 s36, v120, 0
	v_and_b32_e32 v9, 0x7070707, v224
	v_perm_b32 v8, s2, v205, v8
	v_perm_b32 v9, s2, v205, v9
	v_and_or_b32 v8, v92, s4, v8
	v_and_or_b32 v9, v224, s4, v9
	v_perm_b32 v92, v9, v8, s5
	v_perm_b32 v94, v9, v8, s33
	v_perm_b32 v95, v9, v8, s0
	v_perm_b32 v8, v9, v8, s1
	v_pk_fma_f16 v8, v8, s36, v102 op_sel_hi:[1,0,1]
	v_alignbit_b32 v225, v93, v93, 4
	v_pk_fma_f16 v9, v92, s36, v105 op_sel_hi:[1,0,1]
	v_pk_fma_f16 v92, v94, s36, v104 op_sel_hi:[1,0,1]
	v_pk_fma_f16 v94, v95, s36, v103 op_sel_hi:[1,0,1]
	v_and_b32_e32 v95, 0x7070707, v93
	v_and_b32_e32 v102, 0x7070707, v225
	v_perm_b32 v95, s2, v205, v95
	v_perm_b32 v102, s2, v205, v102
	v_and_or_b32 v95, v93, s4, v95
	v_and_or_b32 v93, v225, s4, v102
	v_perm_b32 v102, v93, v95, s5
	v_perm_b32 v103, v93, v95, s33
	v_perm_b32 v104, v93, v95, s0
	v_perm_b32 v93, v93, v95, s1
	v_pk_fma_f16 v95, v102, s36, v101 op_sel_hi:[1,0,1]
	v_readlane_b32 s59, v120, 4
	v_alignbit_b32 v224, v90, v90, 4
	v_pk_fma_f16 v100, v103, s36, v100 op_sel_hi:[1,0,1]
	v_pk_fma_f16 v99, v104, s36, v99 op_sel_hi:[1,0,1]
	v_pk_fma_f16 v7, v93, s36, v15 op_sel_hi:[1,0,1]
	v_and_b32_e32 v93, 0x7070707, v90
	v_and_b32_e32 v101, 0x7070707, v224
	v_perm_b32 v93, s2, v205, v93
	v_perm_b32 v101, s2, v205, v101
	v_and_or_b32 v93, v90, s4, v93
	v_and_or_b32 v90, v224, s4, v101
	v_perm_b32 v103, v90, v93, s0
	v_perm_b32 v101, v90, v93, s5
	v_perm_b32 v102, v90, v93, s33
	v_perm_b32 v90, v90, v93, s1
	v_pk_fma_f16 v93, v103, s59, v94 op_sel_hi:[1,0,1]
	v_alignbit_b32 v225, v91, v91, 4
	v_pk_fma_f16 v8, v90, s59, v8 op_sel_hi:[1,0,1]
	v_and_b32_e32 v90, 0x7070707, v91
	v_and_b32_e32 v94, 0x7070707, v225
	v_pk_fma_f16 v9, v101, s59, v9 op_sel_hi:[1,0,1]
	v_perm_b32 v90, s2, v205, v90
	v_perm_b32 v94, s2, v205, v94
	v_and_or_b32 v90, v91, s4, v90
	v_and_or_b32 v91, v225, s4, v94
	v_pk_fma_f16 v92, v102, s59, v92 op_sel_hi:[1,0,1]
	v_perm_b32 v94, v91, v90, s5
	v_perm_b32 v102, v91, v90, s0
	v_perm_b32 v101, v91, v90, s33
	v_perm_b32 v90, v91, v90, s1
	v_pk_fma_f16 v91, v94, s59, v95 op_sel_hi:[1,0,1]
	v_pk_fma_f16 v95, v102, s59, v99 op_sel_hi:[1,0,1]
	v_readlane_b32 s60, v120, 8
	v_alignbit_b32 v224, v88, v88, 4
	v_pk_fma_f16 v94, v101, s59, v100 op_sel_hi:[1,0,1]
	v_pk_fma_f16 v7, v90, s59, v7 op_sel_hi:[1,0,1]
	v_and_b32_e32 v90, 0x7070707, v88
	v_and_b32_e32 v99, 0x7070707, v224
	v_perm_b32 v90, s2, v205, v90
	v_perm_b32 v99, s2, v205, v99
	v_and_or_b32 v90, v88, s4, v90
	v_and_or_b32 v88, v224, s4, v99
	v_perm_b32 v100, v88, v90, s33
	v_perm_b32 v101, v88, v90, s0
	v_perm_b32 v99, v88, v90, s5
	v_perm_b32 v88, v88, v90, s1
	v_pk_fma_f16 v90, v100, s60, v92 op_sel_hi:[1,0,1]
	v_pk_fma_f16 v92, v101, s60, v93 op_sel_hi:[1,0,1]
	v_alignbit_b32 v225, v89, v89, 4
	v_pk_fma_f16 v8, v88, s60, v8 op_sel_hi:[1,0,1]
	v_and_b32_e32 v88, 0x7070707, v89
	v_and_b32_e32 v93, 0x7070707, v225
	v_pk_fma_f16 v9, v99, s60, v9 op_sel_hi:[1,0,1]
	v_perm_b32 v88, s2, v205, v88
	v_perm_b32 v93, s2, v205, v93
	v_and_or_b32 v88, v89, s4, v88
	v_and_or_b32 v89, v225, s4, v93
	v_perm_b32 v93, v89, v88, s5
	v_perm_b32 v99, v89, v88, s33
	v_perm_b32 v100, v89, v88, s0
	v_perm_b32 v88, v89, v88, s1
	v_pk_fma_f16 v89, v93, s60, v91 op_sel_hi:[1,0,1]
	v_pk_fma_f16 v91, v99, s60, v94 op_sel_hi:[1,0,1]
	v_readlane_b32 s36, v120, 12
	v_alignbit_b32 v224, v86, v86, 4
	v_pk_fma_f16 v93, v100, s60, v95 op_sel_hi:[1,0,1]
	v_pk_fma_f16 v7, v88, s60, v7 op_sel_hi:[1,0,1]
	v_and_b32_e32 v88, 0x7070707, v86
	v_and_b32_e32 v94, 0x7070707, v224
	v_perm_b32 v88, s2, v205, v88
	v_perm_b32 v94, s2, v205, v94
	v_and_or_b32 v88, v86, s4, v88
	v_and_or_b32 v86, v224, s4, v94
	v_perm_b32 v95, v86, v88, s33
	v_perm_b32 v99, v86, v88, s0
	v_perm_b32 v94, v86, v88, s5
	v_perm_b32 v86, v86, v88, s1
	v_pk_fma_f16 v88, v95, s36, v90 op_sel_hi:[1,0,1]
	v_pk_fma_f16 v90, v99, s36, v92 op_sel_hi:[1,0,1]
	v_alignbit_b32 v225, v87, v87, 4
	v_pk_fma_f16 v8, v86, s36, v8 op_sel_hi:[1,0,1]
	v_and_b32_e32 v86, 0x7070707, v87
	v_and_b32_e32 v92, 0x7070707, v225
	v_pk_fma_f16 v9, v94, s36, v9 op_sel_hi:[1,0,1]
	v_perm_b32 v86, s2, v205, v86
	v_perm_b32 v92, s2, v205, v92
	v_and_or_b32 v86, v87, s4, v86
	v_and_or_b32 v87, v225, s4, v92
	v_perm_b32 v92, v87, v86, s5
	v_perm_b32 v94, v87, v86, s33
	v_perm_b32 v95, v87, v86, s0
	v_perm_b32 v86, v87, v86, s1
	v_pk_fma_f16 v87, v92, s36, v89 op_sel_hi:[1,0,1]
	v_readlane_b32 s59, v120, 16
	v_alignbit_b32 v224, v84, v84, 4
	v_pk_fma_f16 v89, v94, s36, v91 op_sel_hi:[1,0,1]
	v_pk_fma_f16 v91, v95, s36, v93 op_sel_hi:[1,0,1]
	v_pk_fma_f16 v7, v86, s36, v7 op_sel_hi:[1,0,1]
	v_and_b32_e32 v86, 0x7070707, v84
	v_and_b32_e32 v92, 0x7070707, v224
	v_perm_b32 v86, s2, v205, v86
	v_perm_b32 v92, s2, v205, v92
	v_and_or_b32 v86, v84, s4, v86
	v_and_or_b32 v84, v224, s4, v92
	v_perm_b32 v93, v84, v86, s33
	v_perm_b32 v94, v84, v86, s0
	v_perm_b32 v92, v84, v86, s5
	v_perm_b32 v84, v84, v86, s1
	v_pk_fma_f16 v86, v93, s59, v88 op_sel_hi:[1,0,1]
	v_pk_fma_f16 v88, v94, s59, v90 op_sel_hi:[1,0,1]
	v_alignbit_b32 v225, v85, v85, 4
	v_pk_fma_f16 v8, v84, s59, v8 op_sel_hi:[1,0,1]
	v_and_b32_e32 v84, 0x7070707, v85
	v_and_b32_e32 v90, 0x7070707, v225
	v_pk_fma_f16 v9, v92, s59, v9 op_sel_hi:[1,0,1]
	v_perm_b32 v84, s2, v205, v84
	v_perm_b32 v90, s2, v205, v90
	v_and_or_b32 v84, v85, s4, v84
	v_and_or_b32 v85, v225, s4, v90
	v_perm_b32 v90, v85, v84, s5
	v_perm_b32 v92, v85, v84, s33
	v_perm_b32 v93, v85, v84, s0
	v_perm_b32 v84, v85, v84, s1
	v_pk_fma_f16 v85, v90, s59, v87 op_sel_hi:[1,0,1]
	v_readlane_b32 s60, v120, 20
	v_alignbit_b32 v224, v82, v82, 4
	v_pk_fma_f16 v87, v92, s59, v89 op_sel_hi:[1,0,1]
	v_pk_fma_f16 v89, v93, s59, v91 op_sel_hi:[1,0,1]
	v_pk_fma_f16 v7, v84, s59, v7 op_sel_hi:[1,0,1]
	v_and_b32_e32 v84, 0x7070707, v82
	v_and_b32_e32 v90, 0x7070707, v224
	v_perm_b32 v84, s2, v205, v84
	v_perm_b32 v90, s2, v205, v90
	v_and_or_b32 v84, v82, s4, v84
	v_and_or_b32 v82, v224, s4, v90
	v_perm_b32 v91, v82, v84, s33
	v_perm_b32 v92, v82, v84, s0
	v_perm_b32 v90, v82, v84, s5
	v_perm_b32 v82, v82, v84, s1
	v_pk_fma_f16 v84, v91, s60, v86 op_sel_hi:[1,0,1]
	v_pk_fma_f16 v86, v92, s60, v88 op_sel_hi:[1,0,1]
	v_alignbit_b32 v225, v83, v83, 4
	v_pk_fma_f16 v8, v82, s60, v8 op_sel_hi:[1,0,1]
	v_and_b32_e32 v82, 0x7070707, v83
	v_and_b32_e32 v88, 0x7070707, v225
	v_pk_fma_f16 v9, v90, s60, v9 op_sel_hi:[1,0,1]
	v_perm_b32 v82, s2, v205, v82
	v_perm_b32 v88, s2, v205, v88
	v_and_or_b32 v82, v83, s4, v82
	v_and_or_b32 v83, v225, s4, v88
	v_perm_b32 v88, v83, v82, s5
	v_perm_b32 v90, v83, v82, s33
	v_perm_b32 v91, v83, v82, s0
	v_perm_b32 v82, v83, v82, s1
	v_pk_fma_f16 v83, v88, s60, v85 op_sel_hi:[1,0,1]
	v_readlane_b32 s36, v120, 24
	v_alignbit_b32 v224, v80, v80, 4
	v_pk_fma_f16 v85, v90, s60, v87 op_sel_hi:[1,0,1]
	v_pk_fma_f16 v87, v91, s60, v89 op_sel_hi:[1,0,1]
	v_pk_fma_f16 v7, v82, s60, v7 op_sel_hi:[1,0,1]
	v_and_b32_e32 v82, 0x7070707, v80
	v_and_b32_e32 v88, 0x7070707, v224
	v_perm_b32 v82, s2, v205, v82
	v_perm_b32 v88, s2, v205, v88
	v_and_or_b32 v82, v80, s4, v82
	v_and_or_b32 v80, v224, s4, v88
	v_perm_b32 v89, v80, v82, s33
	v_perm_b32 v90, v80, v82, s0
	v_perm_b32 v88, v80, v82, s5
	v_perm_b32 v80, v80, v82, s1
	v_pk_fma_f16 v82, v89, s36, v84 op_sel_hi:[1,0,1]
	v_pk_fma_f16 v84, v90, s36, v86 op_sel_hi:[1,0,1]
	v_alignbit_b32 v225, v81, v81, 4
	v_pk_fma_f16 v8, v80, s36, v8 op_sel_hi:[1,0,1]
	v_and_b32_e32 v80, 0x7070707, v81
	v_and_b32_e32 v86, 0x7070707, v225
	v_pk_fma_f16 v9, v88, s36, v9 op_sel_hi:[1,0,1]
	v_perm_b32 v80, s2, v205, v80
	v_perm_b32 v86, s2, v205, v86
	v_and_or_b32 v80, v81, s4, v80
	v_and_or_b32 v81, v225, s4, v86
	v_perm_b32 v86, v81, v80, s5
	v_perm_b32 v88, v81, v80, s33
	v_perm_b32 v89, v81, v80, s0
	v_perm_b32 v80, v81, v80, s1
	v_pk_fma_f16 v81, v86, s36, v83 op_sel_hi:[1,0,1]
	v_readlane_b32 s59, v120, 28
	v_alignbit_b32 v224, v78, v78, 4
	v_pk_fma_f16 v83, v88, s36, v85 op_sel_hi:[1,0,1]
	v_pk_fma_f16 v85, v89, s36, v87 op_sel_hi:[1,0,1]
	v_pk_fma_f16 v7, v80, s36, v7 op_sel_hi:[1,0,1]
	v_and_b32_e32 v80, 0x7070707, v78
	v_and_b32_e32 v86, 0x7070707, v224
	v_perm_b32 v80, s2, v205, v80
	v_perm_b32 v86, s2, v205, v86
	v_and_or_b32 v80, v78, s4, v80
	v_and_or_b32 v78, v224, s4, v86
	v_perm_b32 v87, v78, v80, s33
	v_perm_b32 v88, v78, v80, s0
	v_perm_b32 v86, v78, v80, s5
	v_perm_b32 v78, v78, v80, s1
	v_pk_fma_f16 v80, v87, s59, v82 op_sel_hi:[1,0,1]
	v_pk_fma_f16 v82, v88, s59, v84 op_sel_hi:[1,0,1]
	v_alignbit_b32 v225, v79, v79, 4
	v_pk_fma_f16 v8, v78, s59, v8 op_sel_hi:[1,0,1]
	v_and_b32_e32 v78, 0x7070707, v79
	v_and_b32_e32 v84, 0x7070707, v225
	v_pk_fma_f16 v9, v86, s59, v9 op_sel_hi:[1,0,1]
	v_perm_b32 v78, s2, v205, v78
	v_perm_b32 v84, s2, v205, v84
	v_and_or_b32 v78, v79, s4, v78
	v_and_or_b32 v79, v225, s4, v84
	v_perm_b32 v84, v79, v78, s5
	v_perm_b32 v86, v79, v78, s33
	v_perm_b32 v87, v79, v78, s0
	v_perm_b32 v78, v79, v78, s1
	v_pk_fma_f16 v79, v84, s59, v81 op_sel_hi:[1,0,1]
	v_readlane_b32 s60, v120, 32
	v_alignbit_b32 v224, v76, v76, 4
	v_pk_fma_f16 v81, v86, s59, v83 op_sel_hi:[1,0,1]
	v_pk_fma_f16 v83, v87, s59, v85 op_sel_hi:[1,0,1]
	v_pk_fma_f16 v7, v78, s59, v7 op_sel_hi:[1,0,1]
	v_and_b32_e32 v78, 0x7070707, v76
	v_and_b32_e32 v84, 0x7070707, v224
	v_perm_b32 v78, s2, v205, v78
	v_perm_b32 v84, s2, v205, v84
	v_and_or_b32 v78, v76, s4, v78
	v_and_or_b32 v76, v224, s4, v84
	v_perm_b32 v85, v76, v78, s33
	v_perm_b32 v86, v76, v78, s0
	v_perm_b32 v84, v76, v78, s5
	v_perm_b32 v76, v76, v78, s1
	v_pk_fma_f16 v78, v85, s60, v80 op_sel_hi:[1,0,1]
	v_pk_fma_f16 v80, v86, s60, v82 op_sel_hi:[1,0,1]
	v_alignbit_b32 v225, v77, v77, 4
	v_pk_fma_f16 v8, v76, s60, v8 op_sel_hi:[1,0,1]
	v_and_b32_e32 v76, 0x7070707, v77
	v_and_b32_e32 v82, 0x7070707, v225
	v_pk_fma_f16 v9, v84, s60, v9 op_sel_hi:[1,0,1]
	v_perm_b32 v76, s2, v205, v76
	v_perm_b32 v82, s2, v205, v82
	v_and_or_b32 v76, v77, s4, v76
	v_and_or_b32 v77, v225, s4, v82
	v_perm_b32 v82, v77, v76, s5
	v_perm_b32 v84, v77, v76, s33
	v_perm_b32 v85, v77, v76, s0
	v_perm_b32 v76, v77, v76, s1
	v_pk_fma_f16 v77, v82, s60, v79 op_sel_hi:[1,0,1]
	v_readlane_b32 s36, v120, 36
	v_alignbit_b32 v224, v70, v70, 4
	v_pk_fma_f16 v79, v84, s60, v81 op_sel_hi:[1,0,1]
	v_pk_fma_f16 v81, v85, s60, v83 op_sel_hi:[1,0,1]
	v_pk_fma_f16 v7, v76, s60, v7 op_sel_hi:[1,0,1]
	v_and_b32_e32 v76, 0x7070707, v70
	v_and_b32_e32 v82, 0x7070707, v224
	v_perm_b32 v76, s2, v205, v76
	v_perm_b32 v82, s2, v205, v82
	v_and_or_b32 v76, v70, s4, v76
	v_and_or_b32 v70, v224, s4, v82
	v_perm_b32 v83, v70, v76, s33
	v_perm_b32 v84, v70, v76, s0
	v_perm_b32 v82, v70, v76, s5
	v_perm_b32 v70, v70, v76, s1
	v_pk_fma_f16 v76, v83, s36, v78 op_sel_hi:[1,0,1]
	v_pk_fma_f16 v78, v84, s36, v80 op_sel_hi:[1,0,1]
	v_alignbit_b32 v225, v71, v71, 4
	v_pk_fma_f16 v8, v70, s36, v8 op_sel_hi:[1,0,1]
	v_and_b32_e32 v70, 0x7070707, v71
	v_and_b32_e32 v80, 0x7070707, v225
	v_pk_fma_f16 v9, v82, s36, v9 op_sel_hi:[1,0,1]
	v_perm_b32 v70, s2, v205, v70
	v_perm_b32 v80, s2, v205, v80
	v_and_or_b32 v70, v71, s4, v70
	v_and_or_b32 v71, v225, s4, v80
	v_perm_b32 v80, v71, v70, s5
	v_perm_b32 v82, v71, v70, s33
	v_perm_b32 v83, v71, v70, s0
	v_perm_b32 v70, v71, v70, s1
	v_pk_fma_f16 v71, v80, s36, v77 op_sel_hi:[1,0,1]
	v_readlane_b32 s59, v120, 40
	v_alignbit_b32 v224, v66, v66, 4
	v_pk_fma_f16 v77, v82, s36, v79 op_sel_hi:[1,0,1]
	v_pk_fma_f16 v79, v83, s36, v81 op_sel_hi:[1,0,1]
	v_pk_fma_f16 v7, v70, s36, v7 op_sel_hi:[1,0,1]
	v_and_b32_e32 v70, 0x7070707, v66
	v_and_b32_e32 v80, 0x7070707, v224
	v_perm_b32 v70, s2, v205, v70
	v_perm_b32 v80, s2, v205, v80
	v_and_or_b32 v70, v66, s4, v70
	v_and_or_b32 v66, v224, s4, v80
	v_perm_b32 v81, v66, v70, s33
	v_perm_b32 v82, v66, v70, s0
	v_perm_b32 v80, v66, v70, s5
	v_perm_b32 v66, v66, v70, s1
	v_pk_fma_f16 v70, v81, s59, v76 op_sel_hi:[1,0,1]
	v_pk_fma_f16 v76, v82, s59, v78 op_sel_hi:[1,0,1]
	v_alignbit_b32 v225, v67, v67, 4
	v_pk_fma_f16 v8, v66, s59, v8 op_sel_hi:[1,0,1]
	v_and_b32_e32 v66, 0x7070707, v67
	v_and_b32_e32 v78, 0x7070707, v225
	v_pk_fma_f16 v9, v80, s59, v9 op_sel_hi:[1,0,1]
	v_perm_b32 v66, s2, v205, v66
	v_perm_b32 v78, s2, v205, v78
	v_and_or_b32 v66, v67, s4, v66
	v_and_or_b32 v67, v225, s4, v78
	v_perm_b32 v78, v67, v66, s5
	v_perm_b32 v80, v67, v66, s33
	v_perm_b32 v81, v67, v66, s0
	v_perm_b32 v66, v67, v66, s1
	v_pk_fma_f16 v67, v78, s59, v71 op_sel_hi:[1,0,1]
	v_readlane_b32 s60, v120, 44
	v_alignbit_b32 v224, v72, v72, 4
	v_pk_fma_f16 v71, v80, s59, v77 op_sel_hi:[1,0,1]
	v_pk_fma_f16 v77, v81, s59, v79 op_sel_hi:[1,0,1]
	v_pk_fma_f16 v7, v66, s59, v7 op_sel_hi:[1,0,1]
	v_and_b32_e32 v66, 0x7070707, v72
	v_and_b32_e32 v78, 0x7070707, v224
	v_perm_b32 v66, s2, v205, v66
	v_perm_b32 v78, s2, v205, v78
	v_and_or_b32 v66, v72, s4, v66
	v_and_or_b32 v72, v224, s4, v78
	v_perm_b32 v80, v72, v66, s0
	v_perm_b32 v78, v72, v66, s5
	v_perm_b32 v79, v72, v66, s33
	v_perm_b32 v66, v72, v66, s1
	v_pk_fma_f16 v72, v80, s60, v76 op_sel_hi:[1,0,1]
	v_alignbit_b32 v225, v73, v73, 4
	v_pk_fma_f16 v8, v66, s60, v8 op_sel_hi:[1,0,1]
	v_and_b32_e32 v66, 0x7070707, v73
	v_and_b32_e32 v76, 0x7070707, v225
	v_pk_fma_f16 v9, v78, s60, v9 op_sel_hi:[1,0,1]
	v_perm_b32 v66, s2, v205, v66
	v_perm_b32 v76, s2, v205, v76
	v_and_or_b32 v66, v73, s4, v66
	v_and_or_b32 v73, v225, s4, v76
	v_perm_b32 v76, v73, v66, s5
	v_pk_fma_f16 v70, v79, s60, v70 op_sel_hi:[1,0,1]
	v_perm_b32 v78, v73, v66, s33
	v_perm_b32 v79, v73, v66, s0
	v_perm_b32 v66, v73, v66, s1
	v_pk_fma_f16 v67, v76, s60, v67 op_sel_hi:[1,0,1]
	v_readlane_b32 s36, v120, 48
	v_alignbit_b32 v224, v68, v68, 4
	v_pk_fma_f16 v71, v78, s60, v71 op_sel_hi:[1,0,1]
	v_pk_fma_f16 v73, v79, s60, v77 op_sel_hi:[1,0,1]
	v_pk_fma_f16 v7, v66, s60, v7 op_sel_hi:[1,0,1]
	v_and_b32_e32 v66, 0x7070707, v68
	v_and_b32_e32 v76, 0x7070707, v224
	v_perm_b32 v66, s2, v205, v66
	v_perm_b32 v76, s2, v205, v76
	v_and_or_b32 v66, v68, s4, v66
	v_and_or_b32 v68, v224, s4, v76
	v_perm_b32 v77, v68, v66, s33
	v_perm_b32 v78, v68, v66, s0
	v_perm_b32 v76, v68, v66, s5
	v_perm_b32 v66, v68, v66, s1
	v_pk_fma_f16 v68, v77, s36, v70 op_sel_hi:[1,0,1]
	v_pk_fma_f16 v70, v78, s36, v72 op_sel_hi:[1,0,1]
	v_alignbit_b32 v225, v69, v69, 4
	v_pk_fma_f16 v8, v66, s36, v8 op_sel_hi:[1,0,1]
	v_and_b32_e32 v66, 0x7070707, v69
	v_and_b32_e32 v72, 0x7070707, v225
	v_pk_fma_f16 v9, v76, s36, v9 op_sel_hi:[1,0,1]
	v_perm_b32 v66, s2, v205, v66
	v_perm_b32 v72, s2, v205, v72
	v_and_or_b32 v66, v69, s4, v66
	v_and_or_b32 v69, v225, s4, v72
	v_perm_b32 v72, v69, v66, s5
	v_perm_b32 v76, v69, v66, s33
	v_perm_b32 v77, v69, v66, s0
	v_perm_b32 v66, v69, v66, s1
	v_pk_fma_f16 v67, v72, s36, v67 op_sel_hi:[1,0,1]
	v_readlane_b32 s59, v120, 52
	v_alignbit_b32 v224, v64, v64, 4
	v_pk_fma_f16 v69, v76, s36, v71 op_sel_hi:[1,0,1]
	v_pk_fma_f16 v71, v77, s36, v73 op_sel_hi:[1,0,1]
	v_pk_fma_f16 v7, v66, s36, v7 op_sel_hi:[1,0,1]
	v_and_b32_e32 v66, 0x7070707, v64
	v_and_b32_e32 v72, 0x7070707, v224
	v_perm_b32 v66, s2, v205, v66
	v_perm_b32 v72, s2, v205, v72
	v_and_or_b32 v66, v64, s4, v66
	v_and_or_b32 v64, v224, s4, v72
	v_perm_b32 v73, v64, v66, s33
	v_perm_b32 v76, v64, v66, s0
	v_perm_b32 v72, v64, v66, s5
	v_perm_b32 v64, v64, v66, s1
	v_pk_fma_f16 v66, v73, s59, v68 op_sel_hi:[1,0,1]
	v_pk_fma_f16 v68, v76, s59, v70 op_sel_hi:[1,0,1]
	v_alignbit_b32 v225, v65, v65, 4
	v_pk_fma_f16 v8, v64, s59, v8 op_sel_hi:[1,0,1]
	v_and_b32_e32 v64, 0x7070707, v65
	v_and_b32_e32 v70, 0x7070707, v225
	v_pk_fma_f16 v9, v72, s59, v9 op_sel_hi:[1,0,1]
	v_perm_b32 v64, s2, v205, v64
	v_perm_b32 v70, s2, v205, v70
	v_and_or_b32 v64, v65, s4, v64
	v_and_or_b32 v65, v225, s4, v70
	v_perm_b32 v70, v65, v64, s5
	v_perm_b32 v72, v65, v64, s33
	v_perm_b32 v73, v65, v64, s0
	v_perm_b32 v64, v65, v64, s1
	v_pk_fma_f16 v65, v70, s59, v67 op_sel_hi:[1,0,1]
	v_readlane_b32 s60, v120, 56
	v_alignbit_b32 v224, v62, v62, 4
	v_pk_fma_f16 v67, v72, s59, v69 op_sel_hi:[1,0,1]
	v_pk_fma_f16 v69, v73, s59, v71 op_sel_hi:[1,0,1]
	v_pk_fma_f16 v7, v64, s59, v7 op_sel_hi:[1,0,1]
	v_and_b32_e32 v64, 0x7070707, v62
	v_and_b32_e32 v70, 0x7070707, v224
	v_perm_b32 v64, s2, v205, v64
	v_perm_b32 v70, s2, v205, v70
	v_and_or_b32 v64, v62, s4, v64
	v_and_or_b32 v62, v224, s4, v70
	v_perm_b32 v71, v62, v64, s33
	v_perm_b32 v72, v62, v64, s0
	v_perm_b32 v70, v62, v64, s5
	v_perm_b32 v62, v62, v64, s1
	v_pk_fma_f16 v64, v71, s60, v66 op_sel_hi:[1,0,1]
	v_pk_fma_f16 v66, v72, s60, v68 op_sel_hi:[1,0,1]
	v_alignbit_b32 v225, v63, v63, 4
	v_pk_fma_f16 v8, v62, s60, v8 op_sel_hi:[1,0,1]
	v_and_b32_e32 v62, 0x7070707, v63
	v_and_b32_e32 v68, 0x7070707, v225
	v_pk_fma_f16 v9, v70, s60, v9 op_sel_hi:[1,0,1]
	v_perm_b32 v62, s2, v205, v62
	v_perm_b32 v68, s2, v205, v68
	v_and_or_b32 v62, v63, s4, v62
	v_and_or_b32 v63, v225, s4, v68
	v_perm_b32 v68, v63, v62, s5
	v_perm_b32 v70, v63, v62, s33
	v_perm_b32 v71, v63, v62, s0
	v_perm_b32 v62, v63, v62, s1
	v_pk_fma_f16 v7, v62, s60, v7 op_sel_hi:[1,0,1]
	v_readlane_b32 s36, v120, 60
	v_alignbit_b32 v224, v50, v50, 4
	v_pk_fma_f16 v63, v68, s60, v65 op_sel_hi:[1,0,1]
	v_pk_fma_f16 v65, v70, s60, v67 op_sel_hi:[1,0,1]
	v_pk_fma_f16 v67, v71, s60, v69 op_sel_hi:[1,0,1]
	v_and_b32_e32 v15, 0x7070707, v50
	v_and_b32_e32 v62, 0x7070707, v224
	v_perm_b32 v15, s2, v205, v15
	v_perm_b32 v62, s2, v205, v62
	v_and_or_b32 v15, v50, s4, v15
	v_and_or_b32 v50, v224, s4, v62
	v_perm_b32 v62, v50, v15, s5
	v_perm_b32 v68, v50, v15, s33
	v_perm_b32 v69, v50, v15, s0
	v_perm_b32 v15, v50, v15, s1
	v_pk_fma_f16 v105, v62, s36, v9 op_sel_hi:[1,0,1]
	v_alignbit_b32 v225, v51, v51, 4
	v_pk_fma_f16 v102, v15, s36, v8 op_sel_hi:[1,0,1]
	v_and_b32_e32 v8, 0x7070707, v51
	v_and_b32_e32 v9, 0x7070707, v225
	v_perm_b32 v8, s2, v205, v8
	v_perm_b32 v9, s2, v205, v9
	v_and_or_b32 v8, v51, s4, v8
	v_and_or_b32 v9, v225, s4, v9
	v_perm_b32 v15, v9, v8, s5
	v_perm_b32 v50, v9, v8, s33
	v_perm_b32 v51, v9, v8, s0
	v_perm_b32 v8, v9, v8, s1
	v_pk_fma_f16 v104, v68, s36, v64 op_sel_hi:[1,0,1]
	v_pk_fma_f16 v103, v69, s36, v66 op_sel_hi:[1,0,1]
	v_pk_fma_f16 v101, v15, s36, v63 op_sel_hi:[1,0,1]
	v_pk_fma_f16 v100, v50, s36, v65 op_sel_hi:[1,0,1]
	v_pk_fma_f16 v99, v51, s36, v67 op_sel_hi:[1,0,1]
	v_pk_fma_f16 v15, v8, s36, v7 op_sel_hi:[1,0,1]
	s_add_u32 s66, s10, s64
	s_addc_u32 s67, s11, s65
	global_load_dwordx2 v[92:93], v121, s[66:67]
	s_add_u32 s66, s12, s64
	s_addc_u32 s67, s13, s65
	global_load_dwordx2 v[90:91], v121, s[66:67]
	s_add_u32 s66, s14, s64
	s_addc_u32 s67, s15, s65
	global_load_dwordx2 v[88:89], v121, s[66:67]
	s_add_u32 s66, s16, s64
	s_addc_u32 s67, s17, s65
	global_load_dwordx2 v[86:87], v121, s[66:67]
	s_add_u32 s66, s18, s64
	s_addc_u32 s67, s19, s65
	global_load_dwordx2 v[84:85], v121, s[66:67]
	s_add_u32 s66, s20, s64
	s_addc_u32 s67, s21, s65
	global_load_dwordx2 v[82:83], v121, s[66:67]
	s_add_u32 s66, s22, s64
	s_addc_u32 s67, s23, s65
	global_load_dwordx2 v[80:81], v121, s[66:67]
	s_add_u32 s66, s24, s64
	s_addc_u32 s67, s25, s65
	global_load_dwordx2 v[78:79], v121, s[66:67]
	s_add_u32 s66, s26, s64
	s_addc_u32 s67, s27, s65
	global_load_dwordx2 v[76:77], v121, s[66:67]
	v_readlane_b32 s50, v96, 13
	s_add_u32 s66, s28, s64
	s_addc_u32 s67, s29, s65
	global_load_dwordx2 v[70:71], v121, s[66:67]
	s_add_u32 s66, s30, s62
	s_addc_u32 s67, s31, s63
	global_load_dwordx2 v[40:41], v121, s[66:67]
	s_lshl_b64 s[38:39], s[38:39], 9
	s_ashr_i32 s51, s50, 31
	v_readlane_b32 s52, v96, 14
	s_add_u32 s66, s30, s64
	s_addc_u32 s67, s31, s65
	global_load_dwordx2 v[66:67], v121, s[66:67]
	s_add_u32 s66, s34, s62
	s_addc_u32 s67, s35, s63
	global_load_dwordx2 v[60:61], v121, s[66:67]
	s_add_u32 s66, s34, s64
	s_addc_u32 s67, s35, s65
	global_load_dwordx2 v[72:73], v121, s[66:67]
	s_lshl_b64 s[50:51], s[50:51], 9
	s_ashr_i32 s53, s52, 31
	v_readlane_b32 s54, v96, 15
	s_add_u32 s66, s38, s62
	s_addc_u32 s67, s39, s63
	global_load_dwordx2 v[58:59], v121, s[66:67]
	s_add_u32 s66, s38, s64
	s_addc_u32 s67, s39, s65
	global_load_dwordx2 v[68:69], v121, s[66:67]
	s_lshl_b64 s[52:53], s[52:53], 9
	s_ashr_i32 s55, s54, 31
	s_add_u32 s66, s50, s62
	s_addc_u32 s67, s51, s63
	global_load_dwordx2 v[56:57], v121, s[66:67]
	s_add_u32 s66, s50, s64
	s_addc_u32 s67, s51, s65
	global_load_dwordx2 v[64:65], v121, s[66:67]
	s_lshl_b64 s[54:55], s[54:55], 9
	s_add_u32 s66, s52, s62
	s_addc_u32 s67, s53, s63
	global_load_dwordx2 v[54:55], v121, s[66:67]
	s_add_u32 s66, s52, s64
	s_addc_u32 s67, s53, s65
	global_load_dwordx2 v[62:63], v121, s[66:67]
	s_add_u32 s66, s54, s62
	s_addc_u32 s67, s55, s63
	global_load_dwordx2 v[52:53], v121, s[66:67]
	s_add_u32 s66, s54, s64
	s_addc_u32 s67, s55, s65
	global_load_dwordx2 v[50:51], v121, s[66:67]
	s_cmpk_eq_i32 s56, 0x90
	s_cbranch_scc0 .LBB0_770
	v_lshl_add_u64 v[94:95], v[2:3], 2, v[44:45]
	v_mov_b32_e32 v106, v208
	v_mov_b32_e32 v107, v209
	v_mov_b32_e32 v108, v210
	v_mov_b32_e32 v109, v211
	v_mov_b32_e32 v8, v212
	v_mov_b32_e32 v9, v213
	v_mov_b32_e32 v10, v214
	v_mov_b32_e32 v11, v215
	v_mov_b32_e32 v4, v216
	v_mov_b32_e32 v5, v217
	v_mov_b32_e32 v6, v218
	v_mov_b32_e32 v7, v219
	v_mov_b32_e32 v0, v220
	v_mov_b32_e32 v1, v221
	v_mov_b32_e32 v2, v222
	v_mov_b32_e32 v3, v223
	v_cvt_f32_f16_sdwa v13, v105 dst_sel:DWORD dst_unused:UNUSED_PAD src0_sel:WORD_1
	v_cvt_f32_f16_e32 v12, v105
	s_mov_b32 s12, 0x800000
	v_readlane_b32 s10, v255, 5
	v_readlane_b32 s11, v255, 6
	v_pk_add_f32 v[0:1], v[0:1], v[12:13]
	v_cvt_f32_f16_sdwa v13, v104 dst_sel:DWORD dst_unused:UNUSED_PAD src0_sel:WORD_1
	v_cvt_f32_f16_e32 v12, v104
	v_lshl_add_u64 v[48:49], v[48:49], 0, s[10:11]
	v_pk_add_f32 v[2:3], v[2:3], v[12:13]
	v_cvt_f32_f16_sdwa v13, v103 dst_sel:DWORD dst_unused:UNUSED_PAD src0_sel:WORD_1
	v_cvt_f32_f16_e32 v12, v103
	global_store_dwordx4 v[94:95], v[0:3], off
	v_pk_add_f32 v[4:5], v[4:5], v[12:13]
	v_cvt_f32_f16_sdwa v13, v102 dst_sel:DWORD dst_unused:UNUSED_PAD src0_sel:WORD_1
	v_cvt_f32_f16_e32 v12, v102
	v_mov_b32_e32 v102, v1
	v_mov_b32_e32 v103, v5
	v_pk_mul_f32 v[102:103], v[102:103], v[102:103]
	v_pk_add_f32 v[6:7], v[6:7], v[12:13]
	v_mov_b32_e32 v12, v0
	v_mov_b32_e32 v13, v4
	v_pk_fma_f32 v[12:13], v[12:13], v[12:13], v[102:103]
	v_mov_b32_e32 v102, v2
	v_mov_b32_e32 v103, v6
	v_pk_fma_f32 v[12:13], v[102:103], v[102:103], v[12:13]
	v_mov_b32_e32 v102, v3
	v_mov_b32_e32 v103, v7
	v_pk_fma_f32 v[102:103], v[102:103], v[102:103], v[12:13]
	v_cvt_f32_f16_sdwa v13, v101 dst_sel:DWORD dst_unused:UNUSED_PAD src0_sel:WORD_1
	v_cvt_f32_f16_e32 v12, v101
	v_cvt_f32_f16_sdwa v101, v15 dst_sel:DWORD dst_unused:UNUSED_PAD src0_sel:WORD_1
	global_store_dwordx4 v[94:95], v[4:7], off offset:16
	v_pk_add_f32 v[8:9], v[8:9], v[12:13]
	v_cvt_f32_f16_sdwa v13, v100 dst_sel:DWORD dst_unused:UNUSED_PAD src0_sel:WORD_1
	v_cvt_f32_f16_e32 v12, v100
	v_cvt_f32_f16_e32 v100, v15
	v_pk_add_f32 v[10:11], v[10:11], v[12:13]
	v_cvt_f32_f16_sdwa v13, v99 dst_sel:DWORD dst_unused:UNUSED_PAD src0_sel:WORD_1
	v_cvt_f32_f16_e32 v12, v99
	v_pk_add_f32 v[14:15], v[108:109], v[100:101]
	v_mov_b32_e32 v100, v9
	global_store_dwordx4 v[94:95], v[8:11], off offset:32
	v_pk_add_f32 v[12:13], v[106:107], v[12:13]
	global_store_dwordx4 v[94:95], v[12:15], off offset:48
	v_mov_b32_e32 v101, v13
	v_mov_b32_e32 v94, v8
	v_mov_b32_e32 v95, v12
	v_pk_mul_f32 v[100:101], v[100:101], v[100:101]
	v_add_f32_e32 v99, v102, v103
	v_pk_fma_f32 v[94:95], v[94:95], v[94:95], v[100:101]
	v_mov_b32_e32 v100, v10
	v_mov_b32_e32 v101, v14
	v_pk_fma_f32 v[94:95], v[100:101], v[100:101], v[94:95]
	v_mov_b32_e32 v100, v11
	v_mov_b32_e32 v101, v15
	v_pk_fma_f32 v[94:95], v[100:101], v[100:101], v[94:95]
	global_load_dwordx4 v[100:103], v[46:47], off offset:48
	global_load_dwordx4 v[104:107], v[46:47], off offset:32
	global_load_dwordx4 v[108:111], v[46:47], off offset:16
	global_load_dwordx4 v[112:115], v[46:47], off
	v_add_f32_e32 v94, v99, v94
	v_add_f32_e32 v94, v94, v95
	v_mov_b32_e32 v95, v94
	s_nop 1
	v_permlane32_swap_b32 v95, v94
	s_waitcnt lgkmcnt(0)
	v_add_f32_e32 v94, v94, v95
	v_mov_b32_e32 v95, v94
	s_nop 1
	v_permlane16_swap_b32 v95, v94
	s_waitcnt lgkmcnt(0)
	v_add_f32_e32 v94, v94, v95
	s_nop 1
	v_mov_b32_dpp v95, v94 row_ror:8 row_mask:0xf bank_mask:0xf
	s_waitcnt lgkmcnt(0)
	v_add_f32_e32 v94, v94, v95
	s_nop 1
	v_mov_b32_dpp v95, v94 row_half_mirror row_mask:0xf bank_mask:0xf
	s_nop 1
	v_mov_b32_dpp v95, v95 quad_perm:[3,2,1,0] row_mask:0xf bank_mask:0xf
	s_waitcnt lgkmcnt(0)
	v_add_f32_e32 v94, v94, v95
	s_nop 1
	v_mov_b32_dpp v95, v94 quad_perm:[2,3,0,1] row_mask:0xf bank_mask:0xf
	s_waitcnt lgkmcnt(0)
	v_add_f32_e32 v94, v94, v95
	s_nop 1
	v_mov_b32_dpp v95, v94 quad_perm:[1,0,3,2] row_mask:0xf bank_mask:0xf
	s_waitcnt lgkmcnt(0)
	v_add_f32_e32 v94, v94, v95
	v_fmamk_f32 v94, v94, 0x3a800000, v191
	v_cmp_gt_f32_e32 vcc, s12, v94
	v_mul_f32_e32 v95, 0x4b800000, v94
	s_nop 0
	v_cndmask_b32_e32 v94, v94, v95, vcc
	v_rsq_f32_e32 v94, v94
	s_nop 0
	v_mul_f32_e32 v95, 0x45800000, v94
	v_cndmask_b32_e32 v94, v94, v95, vcc
	v_pk_mul_f32 v[0:1], v[0:1], v[94:95] op_sel_hi:[1,0]
	v_pk_mul_f32 v[2:3], v[2:3], v[94:95] op_sel_hi:[1,0]
	s_waitcnt vmcnt(0)
	v_pk_mul_f32 v[0:1], v[112:113], v[0:1]
	v_pk_mul_f32 v[2:3], v[114:115], v[2:3]
	v_cvt_pk_bf16_f32 v0, v0, v1
	v_cvt_pk_bf16_f32 v1, v2, v3
	v_pk_mul_f32 v[2:3], v[4:5], v[94:95] op_sel_hi:[1,0]
	v_pk_mul_f32 v[4:5], v[6:7], v[94:95] op_sel_hi:[1,0]
	v_pk_mul_f32 v[2:3], v[108:109], v[2:3]
	v_pk_mul_f32 v[4:5], v[110:111], v[4:5]
	v_cvt_pk_bf16_f32 v2, v2, v3
	v_cvt_pk_bf16_f32 v3, v4, v5
	v_pk_mul_f32 v[4:5], v[8:9], v[94:95] op_sel_hi:[1,0]
	v_pk_mul_f32 v[6:7], v[10:11], v[94:95] op_sel_hi:[1,0]
	v_pk_mul_f32 v[4:5], v[104:105], v[4:5]
	v_pk_mul_f32 v[6:7], v[6:7], v[106:107]
	v_cvt_pk_bf16_f32 v4, v4, v5
	v_cvt_pk_bf16_f32 v5, v6, v7
	v_pk_mul_f32 v[6:7], v[12:13], v[94:95] op_sel_hi:[1,0]
	v_pk_mul_f32 v[8:9], v[14:15], v[94:95] op_sel_hi:[1,0]
	v_pk_mul_f32 v[6:7], v[6:7], v[100:101]
	v_pk_mul_f32 v[8:9], v[8:9], v[102:103]
	v_cvt_pk_bf16_f32 v6, v6, v7
	v_cvt_pk_bf16_f32 v7, v8, v9
	global_store_dwordx4 v[74:75], v[0:3], off
	global_store_dwordx4 v[74:75], v[4:7], off offset:16
	s_nop 0
	v_mov_b32_e32 v0, v98
	s_andn2_b64 exec, exec, s[8:9]
	s_cbranch_execnz .LBB0_769
